# baseline (speedup 1.0000x reference)
.Lw2_keep:
	ds_read_b128 v[162:165], v179 offset:192
	s_waitcnt vmcnt(15) lgkmcnt(5)
	v_mfma_f32_32x32x16_f16 v[30:45], v[98:101], v[26:29], v[30:45]
	ds_read_b128 v[22:25], v179 offset:224
	s_waitcnt vmcnt(14) lgkmcnt(5)
	v_mfma_f32_32x32x16_f16 v[30:45], v[114:117], v[46:49], v[30:45]
	ds_read_b128 v[26:29], v179 offset:256
	s_waitcnt vmcnt(13) lgkmcnt(5)
	v_mfma_f32_32x32x16_f16 v[30:45], v[86:89], v[50:53], v[30:45]
	ds_read_b128 v[46:49], v179 offset:288
	s_waitcnt vmcnt(12) lgkmcnt(5)
	v_mfma_f32_32x32x16_f16 v[30:45], v[126:129], v[54:57], v[30:45]
	ds_read_b128 v[50:53], v179 offset:320
	s_waitcnt vmcnt(11) lgkmcnt(5)
	v_mfma_f32_32x32x16_f16 v[30:45], v[90:93], v[58:61], v[30:45]
	ds_read_b128 v[54:57], v179 offset:352
	s_waitcnt vmcnt(10) lgkmcnt(5)
	v_mfma_f32_32x32x16_f16 v[30:45], v[118:121], v[162:165], v[30:45]
	ds_read_b128 v[58:61], v179 offset:384
	s_waitcnt vmcnt(9) lgkmcnt(5)
	v_mfma_f32_32x32x16_f16 v[30:45], v[78:81], v[22:25], v[30:45]
	ds_read_b128 v[162:165], v179 offset:416
	s_waitcnt vmcnt(8) lgkmcnt(5)
	v_mfma_f32_32x32x16_f16 v[30:45], v[102:105], v[26:29], v[30:45]
	ds_read_b128 v[22:25], v179 offset:448
	s_waitcnt vmcnt(7) lgkmcnt(5)
	v_mfma_f32_32x32x16_f16 v[30:45], v[74:77], v[46:49], v[30:45]
	ds_read_b128 v[26:29], v179 offset:480
	s_waitcnt vmcnt(6) lgkmcnt(5)
	v_mfma_f32_32x32x16_f16 v[30:45], v[106:109], v[50:53], v[30:45]
	s_waitcnt vmcnt(5) lgkmcnt(4)
	v_mfma_f32_32x32x16_f16 v[30:45], v[82:85], v[54:57], v[30:45]
	s_waitcnt vmcnt(4) lgkmcnt(3)
	v_mfma_f32_32x32x16_f16 v[30:45], v[110:113], v[58:61], v[30:45]
	v_pk_add_f16 v48, v18, v146
	v_pk_add_f16 v49, v19, v147
	s_nop 0
	v_pk_mul_f16 v46, v20, v148 clamp
	v_pk_mul_f16 v47, v21, v149 clamp
	v_pk_max_f16 v46, v48, v46
	v_pk_max_f16 v47, v49, v47
	ds_write_b64 v189, v[46:47] offset:33792
	s_waitcnt vmcnt(3) lgkmcnt(3)
	v_mfma_f32_32x32x16_f16 v[30:45], v[94:97], v[162:165], v[30:45]
	v_pk_add_f16 v48, v18, v138
	v_pk_add_f16 v49, v19, v139
	s_nop 0
	v_pk_mul_f16 v46, v20, v140 clamp
	v_pk_mul_f16 v47, v21, v141 clamp
	v_pk_max_f16 v46, v48, v46
	v_pk_max_f16 v47, v49, v47
	ds_write_b64 v189, v[46:47] offset:34320
	s_waitcnt vmcnt(2) lgkmcnt(3)
	v_mfma_f32_32x32x16_f16 v[30:45], v[134:137], v[22:25], v[30:45]
	v_pk_add_f16 v48, v18, v150
	v_pk_add_f16 v49, v19, v151
	s_nop 0
	v_pk_mul_f16 v46, v20, v152 clamp
	v_pk_mul_f16 v47, v21, v153 clamp
	v_pk_max_f16 v46, v48, v46
	v_pk_max_f16 v47, v49, v47
	ds_write_b64 v189, v[46:47] offset:34848
	s_waitcnt vmcnt(1) lgkmcnt(3)
	v_mfma_f32_32x32x16_f16 v[30:45], v[130:133], v[26:29], v[30:45]
	v_pk_add_f16 v22, v18, v142
	v_pk_add_f16 v23, v19, v143
	s_nop 0
	v_pk_mul_f16 v18, v20, v144 clamp
	v_pk_mul_f16 v19, v21, v145 clamp
	v_pk_max_f16 v18, v22, v18
	v_pk_max_f16 v19, v23, v19
	ds_write_b64 v189, v[18:19] offset:35376
	global_load_dwordx4 v[162:165], v[154:155], off
	ds_read_b128 v[46:49], v179 offset:16896
	ds_read_b128 v[50:53], v179 offset:16928
	ds_read_b128 v[54:57], v179 offset:16960
	ds_read_b128 v[58:61], v179 offset:16992
	ds_read_b128 v[168:171], v179 offset:17024
	ds_read_b128 v[172:175], v179 offset:17056
	s_nop 0
	v_cvt_pk_f16_f32 v167, v30, v31
	v_cvt_pk_f16_f32 v177, v32, v33
	s_waitcnt lgkmcnt(5)
	v_mfma_f32_32x32x16_f16 v[18:33], v[122:125], v[46:49], v[2:17]
	ds_read_b128 v[180:183], v179 offset:17088
	s_waitcnt lgkmcnt(5)
	v_mfma_f32_32x32x16_f16 v[18:33], v[98:101], v[50:53], v[18:33]
	ds_read_b128 v[184:187], v179 offset:17120
	v_exp_f16_e64 v46, v167 clamp
	v_exp_f16_e64 v47, v177 clamp
	v_exp_f16_sdwa v46, v167 clamp dst_sel:WORD_1 dst_unused:UNUSED_PRESERVE src0_sel:WORD_1
	v_exp_f16_sdwa v47, v177 clamp dst_sel:WORD_1 dst_unused:UNUSED_PRESERVE src0_sel:WORD_1
	s_nop 0
	s_waitcnt lgkmcnt(5)
	v_mfma_f32_32x32x16_f16 v[18:33], v[114:117], v[54:57], v[18:33]
	ds_read_b128 v[190:193], v179 offset:17152
	s_movk_i32 s0, 0x3dc5
	v_mov_b32_e32 v178, 0xbdc5
	v_pk_fma_f16 v47, v47, s0, v178 op_sel_hi:[1,0,0]
	v_pk_fma_f16 v46, v46, s0, v178 op_sel_hi:[1,0,0]
	v_pk_max_f16 v47, v177, v47
	v_pk_max_f16 v46, v167, v46
	s_waitcnt lgkmcnt(5)
	v_mfma_f32_32x32x16_f16 v[18:33], v[86:89], v[58:61], v[18:33]
	ds_read_b128 v[194:197], v179 offset:17184
	v_cvt_pk_f16_f32 v48, v34, v35
	v_cvt_pk_f16_f32 v49, v36, v37
	s_waitcnt lgkmcnt(5)
	v_mfma_f32_32x32x16_f16 v[18:33], v[126:129], v[168:171], v[18:33]
	ds_read_b128 v[34:37], v179 offset:17216
	v_exp_f16_e64 v50, v48 clamp
	v_exp_f16_e64 v51, v49 clamp
	v_exp_f16_sdwa v50, v48 clamp dst_sel:WORD_1 dst_unused:UNUSED_PRESERVE src0_sel:WORD_1
	v_exp_f16_sdwa v51, v49 clamp dst_sel:WORD_1 dst_unused:UNUSED_PRESERVE src0_sel:WORD_1
	s_nop 0
	s_waitcnt lgkmcnt(5)
	v_mfma_f32_32x32x16_f16 v[18:33], v[90:93], v[172:175], v[18:33]
	ds_read_b128 v[168:171], v179 offset:17248
	v_pk_fma_f16 v51, v51, s0, v178 op_sel_hi:[1,0,0]
	v_pk_fma_f16 v50, v50, s0, v178 op_sel_hi:[1,0,0]
	v_pk_max_f16 v49, v49, v51
	v_pk_max_f16 v48, v48, v50
	s_waitcnt lgkmcnt(5)
	v_mfma_f32_32x32x16_f16 v[18:33], v[118:121], v[180:183], v[18:33]
	ds_read_b128 v[172:175], v179 offset:17280
	v_cvt_pk_f16_f32 v167, v38, v39
	v_cvt_pk_f16_f32 v177, v40, v41
	v_mfma_f32_16x16x32_f16 v[58:61], v[70:73], v[46:49], 0
	s_waitcnt lgkmcnt(5)
	v_mfma_f32_32x32x16_f16 v[18:33], v[78:81], v[184:187], v[18:33]
	ds_read_b128 v[38:41], v179 offset:17312
	v_exp_f16_e64 v188, v167 clamp
	v_exp_f16_e64 v198, v177 clamp
	v_exp_f16_sdwa v188, v167 clamp dst_sel:WORD_1 dst_unused:UNUSED_PRESERVE src0_sel:WORD_1
	v_exp_f16_sdwa v198, v177 clamp dst_sel:WORD_1 dst_unused:UNUSED_PRESERVE src0_sel:WORD_1
	s_nop 0
	s_waitcnt lgkmcnt(5)
	v_mfma_f32_32x32x16_f16 v[18:33], v[102:105], v[190:193], v[18:33]
	ds_read_b128 v[180:183], v179 offset:17344
	v_pk_fma_f16 v184, v198, s0, v178 op_sel_hi:[1,0,0]
	s_nop 0
	v_pk_max_f16 v185, v177, v184
	v_pk_fma_f16 v177, v188, s0, v178 op_sel_hi:[1,0,0]
	s_nop 0
	v_pk_max_f16 v184, v167, v177
	s_waitcnt lgkmcnt(5)
	v_mfma_f32_32x32x16_f16 v[18:33], v[74:77], v[194:197], v[18:33]
	ds_read_b128 v[190:193], v179 offset:17376
	v_cvt_pk_f16_f32 v42, v42, v43
	v_cvt_pk_f16_f32 v43, v44, v45
	s_waitcnt lgkmcnt(5)
	v_mfma_f32_32x32x16_f16 v[18:33], v[106:109], v[34:37], v[18:33]
	v_exp_f16_e64 v44, v42 clamp
	v_exp_f16_e64 v45, v43 clamp
	v_exp_f16_sdwa v44, v42 clamp dst_sel:WORD_1 dst_unused:UNUSED_PRESERVE src0_sel:WORD_1
	v_exp_f16_sdwa v45, v43 clamp dst_sel:WORD_1 dst_unused:UNUSED_PRESERVE src0_sel:WORD_1
	s_nop 0
	s_waitcnt lgkmcnt(4)
	v_mfma_f32_32x32x16_f16 v[18:33], v[82:85], v[168:171], v[18:33]
	v_pk_fma_f16 v34, v45, s0, v178 op_sel_hi:[1,0,0]
	s_nop 0
	v_pk_max_f16 v187, v43, v34
	v_pk_fma_f16 v34, v44, s0, v178 op_sel_hi:[1,0,0]
	s_nop 0
	v_pk_max_f16 v186, v42, v34
	s_waitcnt lgkmcnt(3)
	v_mfma_f32_32x32x16_f16 v[18:33], v[110:113], v[172:175], v[18:33]
	v_pk_add_f16 v36, v62, v146
	v_pk_add_f16 v37, v63, v147
	s_nop 0
	v_pk_mul_f16 v34, v64, v148 clamp
	v_pk_mul_f16 v35, v65, v149 clamp
	v_pk_max_f16 v34, v36, v34
	v_pk_max_f16 v35, v37, v35
	ds_write_b64 v189, v[34:35] offset:50688
	v_mfma_f32_16x16x32_f16 v[58:61], v[66:69], v[184:187], v[58:61]
	s_waitcnt lgkmcnt(3)
	v_mfma_f32_32x32x16_f16 v[18:33], v[94:97], v[38:41], v[18:33]
	v_pk_add_f16 v36, v62, v138
	v_pk_add_f16 v37, v63, v139
	s_nop 0
	v_pk_mul_f16 v34, v64, v140 clamp
	v_pk_mul_f16 v35, v65, v141 clamp
	v_pk_max_f16 v34, v36, v34
	v_pk_max_f16 v35, v37, v35
	ds_write_b64 v189, v[34:35] offset:51216
	s_waitcnt lgkmcnt(3)
	v_mfma_f32_32x32x16_f16 v[18:33], v[134:137], v[180:183], v[18:33]
	v_pk_add_f16 v36, v62, v150
	v_pk_add_f16 v37, v63, v151
	s_nop 0
	v_pk_mul_f16 v34, v64, v152 clamp
	v_pk_mul_f16 v35, v65, v153 clamp
	v_pk_max_f16 v34, v36, v34
	v_pk_max_f16 v35, v37, v35
	ds_write_b64 v189, v[34:35] offset:51744
	v_pk_add_f16 v36, v62, v142
	v_pk_add_f16 v37, v63, v143
	s_nop 0
	v_pk_mul_f16 v34, v64, v144 clamp
	v_pk_mul_f16 v35, v65, v145 clamp
	v_pk_max_f16 v34, v36, v34
	v_pk_max_f16 v35, v37, v35
	ds_write_b64 v189, v[34:35] offset:52272
	v_and_b32_e32 v157, 15, v199
	v_lshrrev_b32_e32 v1, 5, v199
	v_lshl_or_b32 v157, v1, 4, v157
	v_bfe_u32 v1, v199, 4, 1
	v_lshlrev_b32_e32 v1, 2, v1
	v_or_b32_e32 v178, s2, v157
	v_mul_lo_u32 v167, v178, 7
	v_add_u32_e32 v170, v167, v1
	v_mov_b32_e32 v34, 0x10800
	v_lshl_add_u32 v206, v170, 2, v34
	v_and_b32_e32 v34, 16, v199
	v_cmp_eq_u32_e64 s[0:1], 0, v34
	v_mov_b32_e32 v34, 0x10808
	v_lshl_add_u32 v34, v167, 2, v34
	v_or_b32_e32 v36, 3, v1
	v_mul_i32_i24_e32 v34, -6, v156
	v_mul_u32_u24_e32 v35, 7, v156
	v_cmp_gt_u32_e64 s[2:3], 6, v36
	v_lshlrev_b32_e32 v171, 2, v167
	v_lshlrev_b32_e32 v172, 2, v36
	s_mov_b32 s5, 0x10800
	v_add3_u32 v36, v171, v172, s5
	ds_write2_b32 v206, v58, v59 offset1:1
	s_and_saveexec_b64 s[2:3], s[0:1]
	ds_write2_b32 v206, v60, v61 offset0:2 offset1:3
	s_or_b64 exec, exec, s[2:3]
	s_waitcnt lgkmcnt(6)
	v_mfma_f32_32x32x16_f16 v[18:33], v[130:133], v[190:193], v[18:33]
	s_sub_i32 s9, 0xff, s28
	s_mul_i32 s9, s9, s28
	s_not_b32 s25, s28
	s_ashr_i32 s9, s9, 1
	s_add_i32 s24, s24, s25
	s_add_i32 s24, s24, s9
	s_mul_i32 s8, s39, 0x1fc0
	s_ashr_i32 s9, s24, 31
	s_mul_hi_u32 s5, s39, 0x1fc0
	s_add_u32 s8, s8, s24
	s_addc_u32 s5, s5, s9
	s_mul_i32 s5, s5, 6
	s_mul_hi_u32 s9, s8, 6
	s_add_i32 s9, s9, s5
	v_add_u32_e32 v34, v34, v0
	s_cmpk_lt_u32 s21, 0xc0
	v_add_u32_e32 v173, v34, v35
	v_lshl_or_b32 v177, v34, 8, v156
	s_mul_i32 s8, s8, 6
	s_cselect_b64 s[24:25], -1, 0
	s_cmpk_gt_u32 s21, 0xbf
	s_waitcnt lgkmcnt(0)
	s_barrier
	s_cbranch_scc1 .LBB1_33
	s_andn2_b64 vcc, exec, s[6:7]
	s_mov_b64 s[6:7], -1
	s_cbranch_vccnz .LBB1_29
	s_movk_i32 s5, 0x60
	v_cmp_gt_u32_e32 vcc, s5, v0
	s_and_saveexec_b64 s[6:7], vcc
	s_cbranch_execz .LBB1_28
	v_lshlrev_b32_e32 v38, 2, v173
	v_add_u32_e32 v46, 0x10800, v38
	ds_read2_b32 v[34:35], v46 offset1:224
	v_add_u32_e32 v36, 0x700, v46
	ds_read2_b32 v[36:37], v36 offset1:224
	v_add_u32_e32 v39, 0x109c0, v38
	v_add_u32_e32 v40, 0x10d40, v38
	v_add_u32_e32 v41, 0x110c0, v38
	v_add_u32_e32 v42, 0x11440, v38
	v_add_u32_e32 v43, 0x117c0, v38
	v_add_u32_e32 v44, 0x11b40, v38
	v_add_u32_e32 v45, 0x11ec0, v38
	v_add_u32_e32 v47, 0x12240, v38
	s_waitcnt lgkmcnt(1)
	s_lshl_b64 s[26:27], s[8:9], 2
	v_add_f32_e32 v34, 0, v34
	v_add_f32_e32 v38, v34, v35
	s_waitcnt lgkmcnt(0)
	v_mov_b64_e32 v[34:35], v[36:37]
	v_add_u32_e32 v36, 0xe00, v46
	ds_read2_b32 v[36:37], v36 offset1:224
	v_add_f32_e32 v34, v38, v34
	v_add_u32_e32 v38, 0x1500, v46
	ds_read2_b32 v[38:39], v38 offset1:224
	v_add_f32_e32 v40, v34, v35
	s_waitcnt lgkmcnt(1)
	v_mov_b64_e32 v[34:35], v[36:37]
	s_add_u32 s26, s10, s26
	v_add_f32_e32 v34, v40, v34
	v_add_f32_e32 v36, v34, v35
	s_waitcnt lgkmcnt(0)
	v_mov_b64_e32 v[34:35], v[38:39]
	s_addc_u32 s27, s11, s27
	v_add_f32_e32 v34, v36, v34
	v_add_f32_e32 v34, v34, v35
	v_fmamk_f32 v34, v34, 0x3eb17218, v176
	v_lshlrev_b32 v35, 2, v0
	global_store_dword v35, v34, s[26:27]

.LBB1_59:
	global_load_dwordx4 v[162:165], v[168:169], off
	s_waitcnt lgkmcnt(5)
	v_mfma_f32_32x32x16_f16 v[34:49], v[122:125], v[50:53], v[2:17]
	ds_read_b128 v[244:247], v179 offset:192
	v_cvt_pk_f16_f32 v166, v18, v19
	v_cvt_pk_f16_f32 v167, v20, v21
	s_waitcnt lgkmcnt(5)
	v_mfma_f32_32x32x16_f16 v[34:49], v[98:101], v[54:57], v[34:49]
	ds_read_b128 v[18:21], v179 offset:224
	v_exp_f16_e64 v50, v166 clamp
	v_exp_f16_e64 v51, v167 clamp
	v_exp_f16_sdwa v50, v166 clamp dst_sel:WORD_1 dst_unused:UNUSED_PRESERVE src0_sel:WORD_1
	v_exp_f16_sdwa v51, v167 clamp dst_sel:WORD_1 dst_unused:UNUSED_PRESERVE src0_sel:WORD_1
	s_nop 0
	s_waitcnt lgkmcnt(5)
	v_mfma_f32_32x32x16_f16 v[34:49], v[114:117], v[58:61], v[34:49]
	ds_read_b128 v[248:251], v179 offset:256
	v_pk_fma_f16 v51, v51, s55, v233 op_sel_hi:[1,0,0]
	v_pk_fma_f16 v50, v50, s55, v233 op_sel_hi:[1,0,0]
	v_pk_max_f16 v51, v167, v51
	v_pk_max_f16 v50, v166, v50
	s_waitcnt lgkmcnt(5)
	v_mfma_f32_32x32x16_f16 v[34:49], v[86:89], v[62:65], v[34:49]
	ds_read_b128 v[252:255], v179 offset:288
	v_cvt_pk_f16_f32 v52, v22, v23
	v_cvt_pk_f16_f32 v53, v24, v25
	s_waitcnt lgkmcnt(5)
	v_mfma_f32_32x32x16_f16 v[34:49], v[126:129], v[170:173], v[34:49]
	ds_read_b128 v[22:25], v179 offset:320
	v_exp_f16_e64 v54, v52 clamp
	v_exp_f16_e64 v55, v53 clamp
	v_exp_f16_sdwa v54, v52 clamp dst_sel:WORD_1 dst_unused:UNUSED_PRESERVE src0_sel:WORD_1
	v_exp_f16_sdwa v55, v53 clamp dst_sel:WORD_1 dst_unused:UNUSED_PRESERVE src0_sel:WORD_1
	s_nop 0
	s_waitcnt lgkmcnt(5)
	v_mfma_f32_32x32x16_f16 v[34:49], v[90:93], v[240:243], v[34:49]
	ds_read_b128 v[170:173], v179 offset:352
	v_pk_fma_f16 v55, v55, s55, v233 op_sel_hi:[1,0,0]
	v_pk_fma_f16 v54, v54, s55, v233 op_sel_hi:[1,0,0]
	v_pk_max_f16 v53, v53, v55
	v_pk_max_f16 v52, v52, v54
	s_waitcnt lgkmcnt(5)
	v_mfma_f32_32x32x16_f16 v[34:49], v[118:121], v[244:247], v[34:49]
	ds_read_b128 v[240:243], v179 offset:384
	v_cvt_pk_f16_f32 v166, v26, v27
	v_cvt_pk_f16_f32 v167, v28, v29
	v_mfma_f32_16x16x32_f16 v[62:65], v[70:73], v[50:53], 0
	s_waitcnt lgkmcnt(5)
	v_mfma_f32_32x32x16_f16 v[34:49], v[78:81], v[18:21], v[34:49]
	ds_read_b128 v[26:29], v179 offset:416
	v_exp_f16_e64 v244, v166 clamp
	v_exp_f16_e64 v245, v167 clamp
	v_exp_f16_sdwa v244, v166 clamp dst_sel:WORD_1 dst_unused:UNUSED_PRESERVE src0_sel:WORD_1
	v_exp_f16_sdwa v245, v167 clamp dst_sel:WORD_1 dst_unused:UNUSED_PRESERVE src0_sel:WORD_1
	s_nop 0
	s_waitcnt lgkmcnt(5)
	v_mfma_f32_32x32x16_f16 v[34:49], v[102:105], v[248:251], v[34:49]
	ds_read_b128 v[18:21], v179 offset:448
	v_pk_fma_f16 v245, v245, s55, v233 op_sel_hi:[1,0,0]
	s_nop 0
	v_pk_max_f16 v245, v167, v245
	v_pk_fma_f16 v167, v244, s55, v233 op_sel_hi:[1,0,0]
	s_nop 0
	v_pk_max_f16 v244, v166, v167
	s_waitcnt lgkmcnt(5)
	v_mfma_f32_32x32x16_f16 v[34:49], v[74:77], v[252:255], v[34:49]
	ds_read_b128 v[248:251], v179 offset:480
	v_cvt_pk_f16_f32 v30, v30, v31
	v_cvt_pk_f16_f32 v31, v32, v33
	s_waitcnt lgkmcnt(5)
	v_mfma_f32_32x32x16_f16 v[34:49], v[106:109], v[22:25], v[34:49]
	v_exp_f16_e64 v32, v30 clamp
	v_exp_f16_e64 v33, v31 clamp
	v_exp_f16_sdwa v32, v30 clamp dst_sel:WORD_1 dst_unused:UNUSED_PRESERVE src0_sel:WORD_1
	v_exp_f16_sdwa v33, v31 clamp dst_sel:WORD_1 dst_unused:UNUSED_PRESERVE src0_sel:WORD_1
	s_nop 0
	s_waitcnt lgkmcnt(4)
	v_mfma_f32_32x32x16_f16 v[34:49], v[82:85], v[170:173], v[34:49]
	v_pk_fma_f16 v22, v33, s55, v233 op_sel_hi:[1,0,0]
	s_nop 0
	v_pk_max_f16 v247, v31, v22
	v_pk_fma_f16 v22, v32, s55, v233 op_sel_hi:[1,0,0]
	s_nop 0
	v_pk_max_f16 v246, v30, v22
	s_waitcnt lgkmcnt(3)
	v_mfma_f32_32x32x16_f16 v[34:49], v[110:113], v[240:243], v[34:49]
	s_waitcnt vmcnt(2)
	v_pk_add_f16 v24, v154, v146
	v_pk_add_f16 v25, v155, v147
	s_nop 0
	v_pk_mul_f16 v22, v156, v148 clamp
	v_pk_mul_f16 v23, v157, v149 clamp
	v_pk_max_f16 v22, v24, v22
	v_pk_max_f16 v23, v25, v23
	ds_write_b64 v189, v[22:23] offset:33792
	v_mfma_f32_16x16x32_f16 v[62:65], v[66:69], v[244:247], v[62:65]
	s_waitcnt lgkmcnt(3)
	v_mfma_f32_32x32x16_f16 v[34:49], v[94:97], v[26:29], v[34:49]
	v_pk_add_f16 v24, v154, v138
	v_pk_add_f16 v25, v155, v139
	s_nop 0
	v_pk_mul_f16 v22, v156, v140 clamp
	v_pk_mul_f16 v23, v157, v141 clamp
	v_pk_max_f16 v22, v24, v22
	v_pk_max_f16 v23, v25, v23
	ds_write_b64 v189, v[22:23] offset:34320
	s_waitcnt lgkmcnt(3)
	v_mfma_f32_32x32x16_f16 v[34:49], v[134:137], v[18:21], v[34:49]
	v_pk_add_f16 v24, v154, v150
	v_pk_add_f16 v25, v155, v151
	s_nop 0
	v_pk_mul_f16 v22, v156, v152 clamp
	v_pk_mul_f16 v23, v157, v153 clamp
	v_pk_max_f16 v22, v24, v22
	v_pk_max_f16 v23, v25, v23
	ds_write_b64 v189, v[22:23] offset:34848
	s_waitcnt lgkmcnt(3)
	v_mfma_f32_32x32x16_f16 v[34:49], v[130:133], v[248:251], v[34:49]
	v_pk_add_f16 v20, v154, v142
	v_pk_add_f16 v21, v155, v143
	s_nop 0
	v_pk_mul_f16 v18, v156, v144 clamp
	v_pk_mul_f16 v19, v157, v145 clamp
	v_pk_max_f16 v18, v20, v18
	v_pk_max_f16 v19, v21, v19
	ds_write_b64 v189, v[18:19] offset:35376
	ds_write2_b32 v229, v62, v63 offset1:1
	s_and_saveexec_b64 s[28:29], s[0:1]
	ds_write2_b32 v229, v64, v65 offset0:2 offset1:3
	s_or_b64 exec, exec, s[28:29]
	v_lshl_add_u64 v[166:167], s[20:21], 4, v[168:169]
	global_load_dwordx4 v[154:157], v[166:167], off
	ds_read_b128 v[50:53], v179 offset:16896
	ds_read_b128 v[54:57], v179 offset:16928
	ds_read_b128 v[58:61], v179 offset:16960
	ds_read_b128 v[62:65], v179 offset:16992
	ds_read_b128 v[168:171], v179 offset:17024
	ds_read_b128 v[240:243], v179 offset:17056
	s_waitcnt lgkmcnt(5)
	v_mfma_f32_32x32x16_f16 v[18:33], v[122:125], v[50:53], v[2:17]
	ds_read_b128 v[244:247], v179 offset:17088
	v_cvt_pk_f16_f32 v172, v34, v35
	v_cvt_pk_f16_f32 v173, v36, v37
	s_waitcnt lgkmcnt(5)
	v_mfma_f32_32x32x16_f16 v[18:33], v[98:101], v[54:57], v[18:33]
	ds_read_b128 v[34:37], v179 offset:17120
	v_exp_f16_e64 v50, v172 clamp
	v_exp_f16_e64 v51, v173 clamp
	v_exp_f16_sdwa v50, v172 clamp dst_sel:WORD_1 dst_unused:UNUSED_PRESERVE src0_sel:WORD_1
	v_exp_f16_sdwa v51, v173 clamp dst_sel:WORD_1 dst_unused:UNUSED_PRESERVE src0_sel:WORD_1
	s_nop 0
	s_waitcnt lgkmcnt(5)
	v_mfma_f32_32x32x16_f16 v[18:33], v[114:117], v[58:61], v[18:33]
	ds_read_b128 v[248:251], v179 offset:17152
	v_pk_fma_f16 v51, v51, s55, v233 op_sel_hi:[1,0,0]
	v_pk_fma_f16 v50, v50, s55, v233 op_sel_hi:[1,0,0]
	v_pk_max_f16 v51, v173, v51
	v_pk_max_f16 v50, v172, v50
	s_waitcnt lgkmcnt(5)
	v_mfma_f32_32x32x16_f16 v[18:33], v[86:89], v[62:65], v[18:33]
	ds_read_b128 v[252:255], v179 offset:17184
	v_cvt_pk_f16_f32 v52, v38, v39
	v_cvt_pk_f16_f32 v53, v40, v41
	s_waitcnt lgkmcnt(5)
	v_mfma_f32_32x32x16_f16 v[18:33], v[126:129], v[168:171], v[18:33]
	ds_read_b128 v[38:41], v179 offset:17216
	v_exp_f16_e64 v54, v52 clamp
	v_exp_f16_e64 v55, v53 clamp
	v_exp_f16_sdwa v54, v52 clamp dst_sel:WORD_1 dst_unused:UNUSED_PRESERVE src0_sel:WORD_1
	v_exp_f16_sdwa v55, v53 clamp dst_sel:WORD_1 dst_unused:UNUSED_PRESERVE src0_sel:WORD_1
	s_nop 0
	s_waitcnt lgkmcnt(5)
	v_mfma_f32_32x32x16_f16 v[18:33], v[90:93], v[240:243], v[18:33]
	ds_read_b128 v[168:171], v179 offset:17248
	v_pk_fma_f16 v55, v55, s55, v233 op_sel_hi:[1,0,0]
	v_pk_fma_f16 v54, v54, s55, v233 op_sel_hi:[1,0,0]
	v_pk_max_f16 v53, v53, v55
	v_pk_max_f16 v52, v52, v54
	s_waitcnt lgkmcnt(5)
	v_mfma_f32_32x32x16_f16 v[18:33], v[118:121], v[244:247], v[18:33]
	ds_read_b128 v[240:243], v179 offset:17280
	v_cvt_pk_f16_f32 v172, v42, v43
	v_cvt_pk_f16_f32 v173, v44, v45
	v_mfma_f32_16x16x32_f16 v[62:65], v[70:73], v[50:53], 0
	s_waitcnt lgkmcnt(5)
	v_mfma_f32_32x32x16_f16 v[18:33], v[78:81], v[34:37], v[18:33]
	ds_read_b128 v[42:45], v179 offset:17312
	v_exp_f16_e64 v244, v172 clamp
	v_exp_f16_e64 v245, v173 clamp
	v_exp_f16_sdwa v244, v172 clamp dst_sel:WORD_1 dst_unused:UNUSED_PRESERVE src0_sel:WORD_1
	v_exp_f16_sdwa v245, v173 clamp dst_sel:WORD_1 dst_unused:UNUSED_PRESERVE src0_sel:WORD_1
	s_nop 0
	s_waitcnt lgkmcnt(5)
	v_mfma_f32_32x32x16_f16 v[18:33], v[102:105], v[248:251], v[18:33]
	ds_read_b128 v[34:37], v179 offset:17344
	v_pk_fma_f16 v245, v245, s55, v233 op_sel_hi:[1,0,0]
	s_nop 0
	v_pk_max_f16 v245, v173, v245
	v_pk_fma_f16 v173, v244, s55, v233 op_sel_hi:[1,0,0]
	s_nop 0
	v_pk_max_f16 v244, v172, v173
	s_waitcnt lgkmcnt(5)
	v_mfma_f32_32x32x16_f16 v[18:33], v[74:77], v[252:255], v[18:33]
	ds_read_b128 v[248:251], v179 offset:17376
	v_cvt_pk_f16_f32 v46, v46, v47
	v_cvt_pk_f16_f32 v47, v48, v49
	s_waitcnt lgkmcnt(5)
	v_mfma_f32_32x32x16_f16 v[18:33], v[106:109], v[38:41], v[18:33]
	v_exp_f16_e64 v48, v46 clamp
	v_exp_f16_e64 v49, v47 clamp
	v_exp_f16_sdwa v48, v46 clamp dst_sel:WORD_1 dst_unused:UNUSED_PRESERVE src0_sel:WORD_1
	v_exp_f16_sdwa v49, v47 clamp dst_sel:WORD_1 dst_unused:UNUSED_PRESERVE src0_sel:WORD_1
	s_nop 0
	s_waitcnt lgkmcnt(4)
	v_mfma_f32_32x32x16_f16 v[18:33], v[82:85], v[168:171], v[18:33]
	v_pk_fma_f16 v38, v49, s55, v233 op_sel_hi:[1,0,0]
	s_nop 0
	v_pk_max_f16 v247, v47, v38
	v_pk_fma_f16 v38, v48, s55, v233 op_sel_hi:[1,0,0]
	s_nop 0
	v_pk_max_f16 v246, v46, v38
	s_waitcnt lgkmcnt(3)
	v_mfma_f32_32x32x16_f16 v[18:33], v[110:113], v[240:243], v[18:33]
	s_waitcnt vmcnt(2)
	v_pk_add_f16 v40, v158, v146
	v_pk_add_f16 v41, v159, v147
	s_nop 0
	v_pk_mul_f16 v38, v160, v148 clamp
	v_pk_mul_f16 v39, v161, v149 clamp
	v_pk_max_f16 v38, v40, v38
	v_pk_max_f16 v39, v41, v39
	ds_write_b64 v189, v[38:39] offset:50688
	v_mfma_f32_16x16x32_f16 v[62:65], v[66:69], v[244:247], v[62:65]
	s_waitcnt lgkmcnt(3)
	v_mfma_f32_32x32x16_f16 v[18:33], v[94:97], v[42:45], v[18:33]
	v_pk_add_f16 v40, v158, v138
	v_pk_add_f16 v41, v159, v139
	s_nop 0
	v_pk_mul_f16 v38, v160, v140 clamp
	v_pk_mul_f16 v39, v161, v141 clamp
	v_pk_max_f16 v38, v40, v38
	v_pk_max_f16 v39, v41, v39
	ds_write_b64 v189, v[38:39] offset:51216
	s_waitcnt lgkmcnt(3)
	v_mfma_f32_32x32x16_f16 v[18:33], v[134:137], v[34:37], v[18:33]
	v_pk_add_f16 v40, v158, v150
	v_pk_add_f16 v41, v159, v151
	s_nop 0
	v_pk_mul_f16 v38, v160, v152 clamp
	v_pk_mul_f16 v39, v161, v153 clamp
	v_pk_max_f16 v38, v40, v38
	v_pk_max_f16 v39, v41, v39
	ds_write_b64 v189, v[38:39] offset:51744
	v_pk_add_f16 v36, v158, v142
	v_pk_add_f16 v37, v159, v143
	s_nop 0
	v_pk_mul_f16 v34, v160, v144 clamp
	v_pk_mul_f16 v35, v161, v145 clamp
	v_pk_max_f16 v34, v36, v34
	v_pk_max_f16 v35, v37, v35
	ds_write_b64 v189, v[34:35] offset:52272
	ds_write2_b32 v206, v62, v63 offset1:1
	s_and_saveexec_b64 s[28:29], s[0:1]
	ds_write2_b32 v206, v64, v65 offset0:2 offset1:3
	s_or_b64 exec, exec, s[28:29]
	s_waitcnt lgkmcnt(6)
	v_mfma_f32_32x32x16_f16 v[18:33], v[130:133], v[248:251], v[18:33]
	s_sub_i32 s28, 0x7d, s31
	s_mul_i32 s28, s28, 6
	s_ashr_i32 s29, s28, 31
	s_add_u32 s26, s26, s28
	s_addc_u32 s27, s27, s29
	s_and_b64 vcc, exec, s[8:9]
	s_waitcnt lgkmcnt(0)
	s_barrier
	ds_read_b128 v[50:53], v179 offset:33792
	ds_read_b128 v[54:57], v179 offset:33824
	ds_read_b128 v[58:61], v179 offset:33856
	ds_read_b128 v[62:65], v179 offset:33888
	s_cbranch_vccnz .LBB1_76
	s_cmp_lg_u32 s41, 0
	s_cbranch_scc0 .LBB1_72
	s_and_saveexec_b64 s[28:29], s[6:7]
	s_cbranch_execz .LBB1_71
	ds_read2_b32 v[34:35], v180 offset1:224
	v_add_u32_e32 v36, 0x700, v180
	ds_read2_b32 v[36:37], v36 offset1:224
	v_add_u32_e32 v38, 0xe00, v180
	s_lshl_b32 s30, s56, 28
	s_waitcnt lgkmcnt(1)
	v_add_f32_e32 v34, 0, v34
	v_add_f32_e32 v40, v34, v35
	ds_read2_b32 v[34:35], v38 offset1:224
	v_add_u32_e32 v38, 0x1500, v180
	ds_read2_b32 v[38:39], v38 offset1:224
	s_waitcnt lgkmcnt(2)
	v_add_f32_e32 v36, v40, v36
	v_add_f32_e32 v36, v36, v37
	s_waitcnt lgkmcnt(1)
	v_add_f32_e32 v34, v36, v34
	s_add_i32 s30, s30, 0xb0000000
	v_add_f32_e32 v34, v34, v35
	s_ashr_i32 s30, s30, 31
	s_waitcnt lgkmcnt(0)
	v_add_f32_e32 v34, v34, v38
	s_and_b32 s30, s30, 0x1800
	v_add_f32_e32 v34, v34, v39
	v_add_u32_e32 v35, s30, v232
	ds_write_b32 v35, v34 offset:384

.LBB1_93:
	v_lshl_add_u64 v[158:159], s[20:21], 4, v[166:167]
	global_load_dwordx4 v[170:173], v[158:159], off
	ds_read_b128 v[166:169], v179 offset:33920
	ds_read_b128 v[240:243], v179 offset:33952
	s_add_i32 s34, s57, 1
	s_waitcnt lgkmcnt(5)
	v_mfma_f32_32x32x16_f16 v[34:49], v[122:125], v[50:53], v[2:17]
	ds_read_b128 v[244:247], v179 offset:33984
	v_cvt_pk_f16_f32 v160, v18, v19
	v_cvt_pk_f16_f32 v161, v20, v21
	s_waitcnt lgkmcnt(5)
	v_mfma_f32_32x32x16_f16 v[34:49], v[98:101], v[54:57], v[34:49]
	ds_read_b128 v[18:21], v179 offset:34016
	v_exp_f16_e64 v50, v160 clamp
	v_exp_f16_e64 v51, v161 clamp
	v_exp_f16_sdwa v50, v160 clamp dst_sel:WORD_1 dst_unused:UNUSED_PRESERVE src0_sel:WORD_1
	v_exp_f16_sdwa v51, v161 clamp dst_sel:WORD_1 dst_unused:UNUSED_PRESERVE src0_sel:WORD_1
	s_nop 0
	s_waitcnt lgkmcnt(5)
	v_mfma_f32_32x32x16_f16 v[34:49], v[114:117], v[58:61], v[34:49]
	ds_read_b128 v[248:251], v179 offset:34048
	v_pk_fma_f16 v51, v51, s55, v233 op_sel_hi:[1,0,0]
	v_pk_fma_f16 v50, v50, s55, v233 op_sel_hi:[1,0,0]
	v_pk_max_f16 v51, v161, v51
	v_pk_max_f16 v50, v160, v50
	s_waitcnt lgkmcnt(5)
	v_mfma_f32_32x32x16_f16 v[34:49], v[86:89], v[62:65], v[34:49]
	ds_read_b128 v[252:255], v179 offset:34080
	v_cvt_pk_f16_f32 v52, v22, v23
	v_cvt_pk_f16_f32 v53, v24, v25
	s_waitcnt lgkmcnt(5)
	v_mfma_f32_32x32x16_f16 v[34:49], v[126:129], v[166:169], v[34:49]
	ds_read_b128 v[22:25], v179 offset:34112
	v_exp_f16_e64 v54, v52 clamp
	v_exp_f16_e64 v55, v53 clamp
	v_exp_f16_sdwa v54, v52 clamp dst_sel:WORD_1 dst_unused:UNUSED_PRESERVE src0_sel:WORD_1
	v_exp_f16_sdwa v55, v53 clamp dst_sel:WORD_1 dst_unused:UNUSED_PRESERVE src0_sel:WORD_1
	s_nop 0
	s_waitcnt lgkmcnt(5)
	v_mfma_f32_32x32x16_f16 v[34:49], v[90:93], v[240:243], v[34:49]
	ds_read_b128 v[166:169], v179 offset:34144
	v_pk_fma_f16 v55, v55, s55, v233 op_sel_hi:[1,0,0]
	v_pk_fma_f16 v54, v54, s55, v233 op_sel_hi:[1,0,0]
	v_pk_max_f16 v53, v53, v55
	v_pk_max_f16 v52, v52, v54
	s_waitcnt lgkmcnt(5)
	v_mfma_f32_32x32x16_f16 v[34:49], v[118:121], v[244:247], v[34:49]
	ds_read_b128 v[240:243], v179 offset:34176
	v_cvt_pk_f16_f32 v160, v26, v27
	v_cvt_pk_f16_f32 v161, v28, v29
	v_mfma_f32_16x16x32_f16 v[62:65], v[70:73], v[50:53], 0
	s_waitcnt lgkmcnt(5)
	v_mfma_f32_32x32x16_f16 v[34:49], v[78:81], v[18:21], v[34:49]
	ds_read_b128 v[26:29], v179 offset:34208
	v_exp_f16_e64 v244, v160 clamp
	v_exp_f16_e64 v245, v161 clamp
	v_exp_f16_sdwa v244, v160 clamp dst_sel:WORD_1 dst_unused:UNUSED_PRESERVE src0_sel:WORD_1
	v_exp_f16_sdwa v245, v161 clamp dst_sel:WORD_1 dst_unused:UNUSED_PRESERVE src0_sel:WORD_1
	s_nop 0
	s_waitcnt lgkmcnt(5)
	v_mfma_f32_32x32x16_f16 v[34:49], v[102:105], v[248:251], v[34:49]
	ds_read_b128 v[18:21], v179 offset:34240
	v_pk_fma_f16 v245, v245, s55, v233 op_sel_hi:[1,0,0]
	s_nop 0
	v_pk_max_f16 v245, v161, v245
	v_pk_fma_f16 v161, v244, s55, v233 op_sel_hi:[1,0,0]
	s_nop 0
	v_pk_max_f16 v244, v160, v161
	s_waitcnt lgkmcnt(5)
	v_mfma_f32_32x32x16_f16 v[34:49], v[74:77], v[252:255], v[34:49]
	ds_read_b128 v[248:251], v179 offset:34272
	v_cvt_pk_f16_f32 v30, v30, v31
	v_cvt_pk_f16_f32 v31, v32, v33
	s_waitcnt lgkmcnt(5)
	v_mfma_f32_32x32x16_f16 v[34:49], v[106:109], v[22:25], v[34:49]
	v_exp_f16_e64 v32, v30 clamp
	v_exp_f16_e64 v33, v31 clamp
	v_exp_f16_sdwa v32, v30 clamp dst_sel:WORD_1 dst_unused:UNUSED_PRESERVE src0_sel:WORD_1
	v_exp_f16_sdwa v33, v31 clamp dst_sel:WORD_1 dst_unused:UNUSED_PRESERVE src0_sel:WORD_1
	s_nop 0
	s_waitcnt lgkmcnt(4)
	v_mfma_f32_32x32x16_f16 v[34:49], v[82:85], v[166:169], v[34:49]
	v_pk_fma_f16 v22, v33, s55, v233 op_sel_hi:[1,0,0]
	s_nop 0
	v_pk_max_f16 v247, v31, v22
	v_pk_fma_f16 v22, v32, s55, v233 op_sel_hi:[1,0,0]
	s_nop 0
	v_pk_max_f16 v246, v30, v22
	s_waitcnt lgkmcnt(3)
	v_mfma_f32_32x32x16_f16 v[34:49], v[110:113], v[240:243], v[34:49]
	s_waitcnt vmcnt(2)
	v_pk_add_f16 v24, v146, v162
	v_pk_add_f16 v25, v147, v163
	s_nop 0
	v_pk_mul_f16 v22, v164, v148 clamp
	v_pk_mul_f16 v23, v165, v149 clamp
	v_pk_max_f16 v22, v24, v22
	v_pk_max_f16 v23, v25, v23
	ds_write_b64 v189, v[22:23]
	v_mfma_f32_16x16x32_f16 v[62:65], v[66:69], v[244:247], v[62:65]
	s_waitcnt lgkmcnt(3)
	v_mfma_f32_32x32x16_f16 v[34:49], v[94:97], v[26:29], v[34:49]
	v_pk_add_f16 v24, v138, v162
	v_pk_add_f16 v25, v139, v163
	s_nop 0
	v_pk_mul_f16 v22, v164, v140 clamp
	v_pk_mul_f16 v23, v165, v141 clamp
	v_pk_max_f16 v22, v24, v22
	v_pk_max_f16 v23, v25, v23
	ds_write_b64 v189, v[22:23] offset:528
	s_waitcnt lgkmcnt(3)
	v_mfma_f32_32x32x16_f16 v[34:49], v[134:137], v[18:21], v[34:49]
	v_pk_add_f16 v24, v150, v162
	v_pk_add_f16 v25, v151, v163
	s_nop 0
	v_pk_mul_f16 v22, v164, v152 clamp
	v_pk_mul_f16 v23, v165, v153 clamp
	v_pk_max_f16 v22, v24, v22
	v_pk_max_f16 v23, v25, v23
	ds_write_b64 v189, v[22:23] offset:1056
	s_waitcnt lgkmcnt(3)
	v_mfma_f32_32x32x16_f16 v[34:49], v[130:133], v[248:251], v[34:49]
	s_waitcnt vmcnt(1)
	v_pk_add_f16 v20, v142, v162
	v_pk_add_f16 v21, v143, v163
	s_nop 0
	v_pk_mul_f16 v18, v164, v144 clamp
	v_pk_mul_f16 v19, v165, v145 clamp
	v_pk_max_f16 v18, v20, v18
	v_pk_max_f16 v19, v21, v19
	ds_write_b64 v189, v[18:19] offset:1584
	ds_write2_b32 v201, v62, v63 offset1:1
	s_and_saveexec_b64 s[30:31], s[0:1]
	ds_write2_b32 v201, v64, v65 offset0:2 offset1:3
	s_or_b64 exec, exec, s[30:31]
	v_lshl_add_u64 v[158:159], s[20:21], 4, v[158:159]
	global_load_dwordx4 v[166:169], v[158:159], off
	ds_read_b128 v[50:53], v179 offset:50688
	ds_read_b128 v[54:57], v179 offset:50720
	ds_read_b128 v[58:61], v179 offset:50752
	ds_read_b128 v[62:65], v179 offset:50784
	ds_read_b128 v[160:163], v179 offset:50816
	ds_read_b128 v[240:243], v179 offset:50848
	s_waitcnt lgkmcnt(5)
	v_mfma_f32_32x32x16_f16 v[18:33], v[122:125], v[50:53], v[2:17]
	ds_read_b128 v[244:247], v179 offset:50880
	v_cvt_pk_f16_f32 v164, v34, v35
	v_cvt_pk_f16_f32 v165, v36, v37
	s_waitcnt lgkmcnt(5)
	v_mfma_f32_32x32x16_f16 v[18:33], v[98:101], v[54:57], v[18:33]
	ds_read_b128 v[34:37], v179 offset:50912
	v_exp_f16_e64 v50, v164 clamp
	v_exp_f16_e64 v51, v165 clamp
	v_exp_f16_sdwa v50, v164 clamp dst_sel:WORD_1 dst_unused:UNUSED_PRESERVE src0_sel:WORD_1
	v_exp_f16_sdwa v51, v165 clamp dst_sel:WORD_1 dst_unused:UNUSED_PRESERVE src0_sel:WORD_1
	s_nop 0
	s_waitcnt lgkmcnt(5)
	v_mfma_f32_32x32x16_f16 v[18:33], v[114:117], v[58:61], v[18:33]
	ds_read_b128 v[248:251], v179 offset:50944
	v_pk_fma_f16 v51, v51, s55, v233 op_sel_hi:[1,0,0]
	v_pk_fma_f16 v50, v50, s55, v233 op_sel_hi:[1,0,0]
	v_pk_max_f16 v51, v165, v51
	v_pk_max_f16 v50, v164, v50
	s_waitcnt lgkmcnt(5)
	v_mfma_f32_32x32x16_f16 v[18:33], v[86:89], v[62:65], v[18:33]
	ds_read_b128 v[252:255], v179 offset:50976
	v_cvt_pk_f16_f32 v52, v38, v39
	v_cvt_pk_f16_f32 v53, v40, v41
	s_waitcnt lgkmcnt(5)
	v_mfma_f32_32x32x16_f16 v[18:33], v[126:129], v[160:163], v[18:33]
	ds_read_b128 v[38:41], v179 offset:51008
	v_exp_f16_e64 v54, v52 clamp
	v_exp_f16_e64 v55, v53 clamp
	v_exp_f16_sdwa v54, v52 clamp dst_sel:WORD_1 dst_unused:UNUSED_PRESERVE src0_sel:WORD_1
	v_exp_f16_sdwa v55, v53 clamp dst_sel:WORD_1 dst_unused:UNUSED_PRESERVE src0_sel:WORD_1
	s_nop 0
	s_waitcnt lgkmcnt(5)
	v_mfma_f32_32x32x16_f16 v[18:33], v[90:93], v[240:243], v[18:33]
	ds_read_b128 v[160:163], v179 offset:51040
	v_pk_fma_f16 v55, v55, s55, v233 op_sel_hi:[1,0,0]
	v_pk_fma_f16 v54, v54, s55, v233 op_sel_hi:[1,0,0]
	v_pk_max_f16 v53, v53, v55
	v_pk_max_f16 v52, v52, v54
	s_waitcnt lgkmcnt(5)
	v_mfma_f32_32x32x16_f16 v[18:33], v[118:121], v[244:247], v[18:33]
	ds_read_b128 v[240:243], v179 offset:51072
	v_cvt_pk_f16_f32 v164, v42, v43
	v_cvt_pk_f16_f32 v165, v44, v45
	v_mfma_f32_16x16x32_f16 v[62:65], v[70:73], v[50:53], 0
	s_waitcnt lgkmcnt(5)
	v_mfma_f32_32x32x16_f16 v[18:33], v[78:81], v[34:37], v[18:33]
	ds_read_b128 v[42:45], v179 offset:51104
	v_exp_f16_e64 v244, v164 clamp
	v_exp_f16_e64 v245, v165 clamp
	v_exp_f16_sdwa v244, v164 clamp dst_sel:WORD_1 dst_unused:UNUSED_PRESERVE src0_sel:WORD_1
	v_exp_f16_sdwa v245, v165 clamp dst_sel:WORD_1 dst_unused:UNUSED_PRESERVE src0_sel:WORD_1
	s_nop 0
	s_waitcnt lgkmcnt(5)
	v_mfma_f32_32x32x16_f16 v[18:33], v[102:105], v[248:251], v[18:33]
	ds_read_b128 v[34:37], v179 offset:51136
	v_pk_fma_f16 v245, v245, s55, v233 op_sel_hi:[1,0,0]
	s_nop 0
	v_pk_max_f16 v245, v165, v245
	v_pk_fma_f16 v165, v244, s55, v233 op_sel_hi:[1,0,0]
	s_nop 0
	v_pk_max_f16 v244, v164, v165
	s_waitcnt lgkmcnt(5)
	v_mfma_f32_32x32x16_f16 v[18:33], v[74:77], v[252:255], v[18:33]
	ds_read_b128 v[248:251], v179 offset:51168
	v_cvt_pk_f16_f32 v46, v46, v47
	v_cvt_pk_f16_f32 v47, v48, v49
	s_waitcnt lgkmcnt(5)
	v_mfma_f32_32x32x16_f16 v[18:33], v[106:109], v[38:41], v[18:33]
	v_exp_f16_e64 v48, v46 clamp
	v_exp_f16_e64 v49, v47 clamp
	v_exp_f16_sdwa v48, v46 clamp dst_sel:WORD_1 dst_unused:UNUSED_PRESERVE src0_sel:WORD_1
	v_exp_f16_sdwa v49, v47 clamp dst_sel:WORD_1 dst_unused:UNUSED_PRESERVE src0_sel:WORD_1
	s_nop 0
	s_waitcnt lgkmcnt(4)
	v_mfma_f32_32x32x16_f16 v[18:33], v[82:85], v[160:163], v[18:33]
	v_pk_fma_f16 v38, v49, s55, v233 op_sel_hi:[1,0,0]
	s_nop 0
	v_pk_max_f16 v247, v47, v38
	v_pk_fma_f16 v38, v48, s55, v233 op_sel_hi:[1,0,0]
	s_nop 0
	v_pk_max_f16 v246, v46, v38
	s_waitcnt lgkmcnt(3)
	v_mfma_f32_32x32x16_f16 v[18:33], v[110:113], v[240:243], v[18:33]
	v_pk_add_f16 v40, v146, v154
	v_pk_add_f16 v41, v147, v155
	s_nop 0
	v_pk_mul_f16 v38, v156, v148 clamp
	v_pk_mul_f16 v39, v157, v149 clamp
	v_pk_max_f16 v38, v40, v38
	v_pk_max_f16 v39, v41, v39
	ds_write_b64 v189, v[38:39] offset:16896
	v_mfma_f32_16x16x32_f16 v[62:65], v[66:69], v[244:247], v[62:65]
	s_waitcnt lgkmcnt(3)
	v_mfma_f32_32x32x16_f16 v[18:33], v[94:97], v[42:45], v[18:33]
	v_pk_add_f16 v40, v138, v154
	v_pk_add_f16 v41, v139, v155
	s_nop 0
	v_pk_mul_f16 v38, v156, v140 clamp
	v_pk_mul_f16 v39, v157, v141 clamp
	v_pk_max_f16 v38, v40, v38
	v_pk_max_f16 v39, v41, v39
	ds_write_b64 v189, v[38:39] offset:17424
	s_waitcnt lgkmcnt(3)
	v_mfma_f32_32x32x16_f16 v[18:33], v[134:137], v[34:37], v[18:33]
	v_pk_add_f16 v40, v150, v154
	v_pk_add_f16 v41, v151, v155
	s_nop 0
	v_pk_mul_f16 v38, v156, v152 clamp
	v_pk_mul_f16 v39, v157, v153 clamp
	v_pk_max_f16 v38, v40, v38
	v_pk_max_f16 v39, v41, v39
	ds_write_b64 v189, v[38:39] offset:17952
	v_pk_add_f16 v36, v142, v154
	v_pk_add_f16 v37, v143, v155
	s_nop 0
	v_pk_mul_f16 v34, v156, v144 clamp
	v_pk_mul_f16 v35, v157, v145 clamp
	v_pk_max_f16 v34, v36, v34
	v_pk_max_f16 v35, v37, v35
	ds_write_b64 v189, v[34:35] offset:18480
	ds_write2_b32 v211, v62, v63 offset1:1
	s_and_saveexec_b64 s[30:31], s[0:1]
	ds_write2_b32 v211, v64, v65 offset0:2 offset1:3
	s_or_b64 exec, exec, s[30:31]
	s_waitcnt lgkmcnt(6)
	v_mfma_f32_32x32x16_f16 v[18:33], v[130:133], v[248:251], v[18:33]
	s_sub_i32 s30, 0x7d, s34
	s_mul_i32 s30, s30, 6
	s_ashr_i32 s31, s30, 31
	s_add_u32 s28, s28, s30
	s_addc_u32 s29, s29, s31
	s_and_b64 vcc, exec, s[8:9]
	s_waitcnt lgkmcnt(0)
	s_barrier
	ds_read_b128 v[50:53], v179
	ds_read_b128 v[54:57], v179 offset:32
	ds_read_b128 v[58:61], v179 offset:64
	ds_read_b128 v[62:65], v179 offset:96
	ds_read_b128 v[162:165], v179 offset:128
	ds_read_b128 v[240:243], v179 offset:160
	s_cbranch_vccnz .LBB1_110
	s_cmp_eq_u32 s41, 0
	s_cbranch_scc1 .LBB1_106
	s_and_saveexec_b64 s[30:31], s[6:7]
	s_cbranch_execz .LBB1_105
	ds_read2_b32 v[34:35], v200 offset1:224
	ds_read2_b32 v[36:37], v234 offset1:224
	ds_read2_b32 v[38:39], v235 offset1:224
	ds_read2_b32 v[40:41], v236 offset1:224
	s_lshl_b32 s35, s56, 28
	s_add_i32 s35, s35, 0xd0000000
	s_ashr_i32 s35, s35, 31
	s_waitcnt lgkmcnt(3)
	v_add_f32_e32 v34, 0, v34
	v_add_f32_e32 v34, v34, v35
	s_waitcnt lgkmcnt(2)
	v_add_f32_e32 v34, v34, v36
	v_add_f32_e32 v34, v34, v37
	s_waitcnt lgkmcnt(1)
	v_add_f32_e32 v34, v34, v38
	v_add_f32_e32 v34, v34, v39
	s_waitcnt lgkmcnt(0)
	v_add_f32_e32 v34, v34, v40
	s_and_b32 s35, s35, 0x1800
	v_add_f32_e32 v34, v34, v41
	v_add_u32_e32 v35, s35, v232
	ds_write_b32 v35, v34 offset:640

.Lw2_sw_skip:
	v_lshl_add_u64 v[154:155], s[20:21], 4, v[154:155]
	global_load_dwordx4 v[162:165], v[154:155], off
	ds_read_b128 v[50:53], v179 offset:16896
	ds_read_b128 v[54:57], v179 offset:16928
	ds_read_b128 v[58:61], v179 offset:16960
	ds_read_b128 v[62:65], v179 offset:16992
	ds_read_b128 v[170:173], v179 offset:17024
	ds_read_b128 v[240:243], v179 offset:17056
	s_waitcnt lgkmcnt(5)
	v_mfma_f32_32x32x16_f16 v[18:33], v[122:125], v[50:53], v[2:17]
	ds_read_b128 v[244:247], v179 offset:17088
	v_cvt_pk_f16_f32 v156, v34, v35
	v_cvt_pk_f16_f32 v157, v36, v37
	s_waitcnt lgkmcnt(5)
	v_mfma_f32_32x32x16_f16 v[18:33], v[98:101], v[54:57], v[18:33]
	ds_read_b128 v[34:37], v179 offset:17120
	v_exp_f16_e64 v50, v156 clamp
	v_exp_f16_e64 v51, v157 clamp
	v_exp_f16_sdwa v50, v156 clamp dst_sel:WORD_1 dst_unused:UNUSED_PRESERVE src0_sel:WORD_1
	v_exp_f16_sdwa v51, v157 clamp dst_sel:WORD_1 dst_unused:UNUSED_PRESERVE src0_sel:WORD_1
	s_nop 0
	s_waitcnt lgkmcnt(5)
	v_mfma_f32_32x32x16_f16 v[18:33], v[114:117], v[58:61], v[18:33]
	ds_read_b128 v[248:251], v179 offset:17152
	v_pk_fma_f16 v51, v51, s55, v233 op_sel_hi:[1,0,0]
	v_pk_fma_f16 v50, v50, s55, v233 op_sel_hi:[1,0,0]
	v_pk_max_f16 v51, v157, v51
	v_pk_max_f16 v50, v156, v50
	s_waitcnt lgkmcnt(5)
	v_mfma_f32_32x32x16_f16 v[18:33], v[86:89], v[62:65], v[18:33]
	ds_read_b128 v[252:255], v179 offset:17184
	v_cvt_pk_f16_f32 v52, v38, v39
	v_cvt_pk_f16_f32 v53, v40, v41
	s_waitcnt lgkmcnt(5)
	v_mfma_f32_32x32x16_f16 v[18:33], v[126:129], v[170:173], v[18:33]
	ds_read_b128 v[38:41], v179 offset:17216
	v_exp_f16_e64 v54, v52 clamp
	v_exp_f16_e64 v55, v53 clamp
	v_exp_f16_sdwa v54, v52 clamp dst_sel:WORD_1 dst_unused:UNUSED_PRESERVE src0_sel:WORD_1
	v_exp_f16_sdwa v55, v53 clamp dst_sel:WORD_1 dst_unused:UNUSED_PRESERVE src0_sel:WORD_1
	s_nop 0
	s_waitcnt lgkmcnt(5)
	v_mfma_f32_32x32x16_f16 v[18:33], v[90:93], v[240:243], v[18:33]
	ds_read_b128 v[170:173], v179 offset:17248
	v_pk_fma_f16 v55, v55, s55, v233 op_sel_hi:[1,0,0]
	v_pk_fma_f16 v54, v54, s55, v233 op_sel_hi:[1,0,0]
	v_pk_max_f16 v53, v53, v55
	v_pk_max_f16 v52, v52, v54
	s_waitcnt lgkmcnt(5)
	v_mfma_f32_32x32x16_f16 v[18:33], v[118:121], v[244:247], v[18:33]
	ds_read_b128 v[240:243], v179 offset:17280
	v_cvt_pk_f16_f32 v156, v42, v43
	v_cvt_pk_f16_f32 v157, v44, v45
	v_mfma_f32_16x16x32_f16 v[62:65], v[70:73], v[50:53], 0
	s_waitcnt lgkmcnt(5)
	v_mfma_f32_32x32x16_f16 v[18:33], v[78:81], v[34:37], v[18:33]
	ds_read_b128 v[42:45], v179 offset:17312
	v_exp_f16_e64 v244, v156 clamp
	v_exp_f16_e64 v245, v157 clamp
	v_exp_f16_sdwa v244, v156 clamp dst_sel:WORD_1 dst_unused:UNUSED_PRESERVE src0_sel:WORD_1
	v_exp_f16_sdwa v245, v157 clamp dst_sel:WORD_1 dst_unused:UNUSED_PRESERVE src0_sel:WORD_1
	s_nop 0
	s_waitcnt lgkmcnt(5)
	v_mfma_f32_32x32x16_f16 v[18:33], v[102:105], v[248:251], v[18:33]
	ds_read_b128 v[34:37], v179 offset:17344
	v_pk_fma_f16 v245, v245, s55, v233 op_sel_hi:[1,0,0]
	s_nop 0
	v_pk_max_f16 v245, v157, v245
	v_pk_fma_f16 v157, v244, s55, v233 op_sel_hi:[1,0,0]
	s_nop 0
	v_pk_max_f16 v244, v156, v157
	s_waitcnt lgkmcnt(5)
	v_mfma_f32_32x32x16_f16 v[18:33], v[74:77], v[252:255], v[18:33]
	ds_read_b128 v[248:251], v179 offset:17376
	v_cvt_pk_f16_f32 v46, v46, v47
	v_cvt_pk_f16_f32 v47, v48, v49
	s_waitcnt lgkmcnt(5)
	v_mfma_f32_32x32x16_f16 v[18:33], v[106:109], v[38:41], v[18:33]
	v_exp_f16_e64 v48, v46 clamp
	v_exp_f16_e64 v49, v47 clamp
	v_exp_f16_sdwa v48, v46 clamp dst_sel:WORD_1 dst_unused:UNUSED_PRESERVE src0_sel:WORD_1
	v_exp_f16_sdwa v49, v47 clamp dst_sel:WORD_1 dst_unused:UNUSED_PRESERVE src0_sel:WORD_1
	s_nop 0
	s_waitcnt lgkmcnt(4)
	v_mfma_f32_32x32x16_f16 v[18:33], v[82:85], v[170:173], v[18:33]
	v_pk_fma_f16 v38, v49, s55, v233 op_sel_hi:[1,0,0]
	s_nop 0
	v_pk_max_f16 v247, v47, v38
	v_pk_fma_f16 v38, v48, s55, v233 op_sel_hi:[1,0,0]
	s_nop 0
	v_pk_max_f16 v246, v46, v38
	s_waitcnt lgkmcnt(3)
	v_mfma_f32_32x32x16_f16 v[18:33], v[110:113], v[240:243], v[18:33]
	s_waitcnt vmcnt(2)
	v_pk_add_f16 v40, v166, v146
	v_pk_add_f16 v41, v167, v147
	s_nop 0
	v_pk_mul_f16 v38, v168, v148 clamp
	v_pk_mul_f16 v39, v169, v149 clamp
	v_pk_max_f16 v38, v40, v38
	v_pk_max_f16 v39, v41, v39
	ds_write_b64 v189, v[38:39] offset:50688
	v_mfma_f32_16x16x32_f16 v[62:65], v[66:69], v[244:247], v[62:65]
	s_waitcnt lgkmcnt(3)
	v_mfma_f32_32x32x16_f16 v[18:33], v[94:97], v[42:45], v[18:33]
	v_pk_add_f16 v40, v166, v138
	v_pk_add_f16 v41, v167, v139
	s_nop 0
	v_pk_mul_f16 v38, v168, v140 clamp
	v_pk_mul_f16 v39, v169, v141 clamp
	v_pk_max_f16 v38, v40, v38
	v_pk_max_f16 v39, v41, v39
	ds_write_b64 v189, v[38:39] offset:51216
	s_waitcnt lgkmcnt(3)
	v_mfma_f32_32x32x16_f16 v[18:33], v[134:137], v[34:37], v[18:33]
	v_pk_add_f16 v40, v166, v150
	v_pk_add_f16 v41, v167, v151
	s_nop 0
	v_pk_mul_f16 v38, v168, v152 clamp
	v_pk_mul_f16 v39, v169, v153 clamp
	v_pk_max_f16 v38, v40, v38
	v_pk_max_f16 v39, v41, v39
	ds_write_b64 v189, v[38:39] offset:51744
	v_pk_add_f16 v36, v166, v142
	v_pk_add_f16 v37, v167, v143
	s_nop 0
	v_pk_mul_f16 v34, v168, v144 clamp
	v_pk_mul_f16 v35, v169, v145 clamp
	v_pk_max_f16 v34, v36, v34
	v_pk_max_f16 v35, v37, v35
	ds_write_b64 v189, v[34:35] offset:52272
	ds_write2_b32 v206, v62, v63 offset1:1
	s_and_saveexec_b64 s[30:31], s[0:1]
	ds_write2_b32 v206, v64, v65 offset0:2 offset1:3
	s_or_b64 exec, exec, s[30:31]
	s_waitcnt lgkmcnt(6)
	v_mfma_f32_32x32x16_f16 v[18:33], v[130:133], v[248:251], v[18:33]
	s_add_i32 s34, s34, 1
	s_sub_i32 s30, 0x7d, s34
	s_mul_i32 s30, s30, 6
	s_ashr_i32 s31, s30, 31
	s_add_u32 s28, s28, s30
	s_addc_u32 s29, s29, s31
	s_and_b64 vcc, exec, s[8:9]
	s_waitcnt lgkmcnt(0)
	s_barrier
	ds_read_b128 v[50:53], v179 offset:33792
	ds_read_b128 v[54:57], v179 offset:33824
	ds_read_b128 v[58:61], v179 offset:33856
	ds_read_b128 v[62:65], v179 offset:33888
	ds_read_b128 v[168:171], v179 offset:33920
	ds_read_b128 v[240:243], v179 offset:33952
	s_cbranch_vccnz .LBB1_136
	s_cmp_eq_u32 s41, 0
	s_cbranch_scc1 .LBB1_132
	s_and_saveexec_b64 s[30:31], s[6:7]
	s_cbranch_execz .LBB1_131
	ds_read2_b32 v[34:35], v180 offset1:224
	v_add_u32_e32 v36, 0x700, v180
	ds_read2_b32 v[36:37], v36 offset1:224
	v_add_u32_e32 v38, 0xe00, v180
	s_lshl_b32 s35, s56, 28
	s_waitcnt lgkmcnt(1)
	v_add_f32_e32 v34, 0, v34
	v_add_f32_e32 v40, v34, v35
	ds_read2_b32 v[34:35], v38 offset1:224
	v_add_u32_e32 v38, 0x1500, v180
	ds_read2_b32 v[38:39], v38 offset1:224
	s_waitcnt lgkmcnt(2)
	v_add_f32_e32 v36, v40, v36
	v_add_f32_e32 v36, v36, v37
	s_waitcnt lgkmcnt(1)
	v_add_f32_e32 v34, v36, v34
	s_add_i32 s35, s35, 0xf0000000
	v_add_f32_e32 v34, v34, v35
	s_ashr_i32 s35, s35, 31
	s_waitcnt lgkmcnt(0)
	v_add_f32_e32 v34, v34, v38
	s_and_b32 s35, s35, 0x1800
	v_add_f32_e32 v34, v34, v39
	v_add_u32_e32 v35, s35, v232
	ds_write_b32 v35, v34 offset:896

.LBB1_145:
	v_lshl_add_u64 v[166:167], s[20:21], 4, v[154:155]
	global_load_dwordx4 v[154:157], v[166:167], off
	s_waitcnt lgkmcnt(5)
	v_mfma_f32_32x32x16_f16 v[34:49], v[122:125], v[50:53], v[2:17]
	ds_read_b128 v[244:247], v179 offset:33984
	v_cvt_pk_f16_f32 v172, v18, v19
	v_cvt_pk_f16_f32 v173, v20, v21
	s_waitcnt lgkmcnt(5)
	v_mfma_f32_32x32x16_f16 v[34:49], v[98:101], v[54:57], v[34:49]
	ds_read_b128 v[18:21], v179 offset:34016
	v_exp_f16_e64 v50, v172 clamp
	v_exp_f16_e64 v51, v173 clamp
	v_exp_f16_sdwa v50, v172 clamp dst_sel:WORD_1 dst_unused:UNUSED_PRESERVE src0_sel:WORD_1
	v_exp_f16_sdwa v51, v173 clamp dst_sel:WORD_1 dst_unused:UNUSED_PRESERVE src0_sel:WORD_1
	s_nop 0
	s_waitcnt lgkmcnt(5)
	v_mfma_f32_32x32x16_f16 v[34:49], v[114:117], v[58:61], v[34:49]
	ds_read_b128 v[248:251], v179 offset:34048
	v_pk_fma_f16 v51, v51, s55, v233 op_sel_hi:[1,0,0]
	v_pk_fma_f16 v50, v50, s55, v233 op_sel_hi:[1,0,0]
	v_pk_max_f16 v51, v173, v51
	v_pk_max_f16 v50, v172, v50
	s_waitcnt lgkmcnt(5)
	v_mfma_f32_32x32x16_f16 v[34:49], v[86:89], v[62:65], v[34:49]
	ds_read_b128 v[252:255], v179 offset:34080
	v_cvt_pk_f16_f32 v52, v22, v23
	v_cvt_pk_f16_f32 v53, v24, v25
	s_waitcnt lgkmcnt(5)
	v_mfma_f32_32x32x16_f16 v[34:49], v[126:129], v[168:171], v[34:49]
	ds_read_b128 v[22:25], v179 offset:34112
	v_exp_f16_e64 v54, v52 clamp
	v_exp_f16_e64 v55, v53 clamp
	v_exp_f16_sdwa v54, v52 clamp dst_sel:WORD_1 dst_unused:UNUSED_PRESERVE src0_sel:WORD_1
	v_exp_f16_sdwa v55, v53 clamp dst_sel:WORD_1 dst_unused:UNUSED_PRESERVE src0_sel:WORD_1
	s_nop 0
	s_waitcnt lgkmcnt(5)
	v_mfma_f32_32x32x16_f16 v[34:49], v[90:93], v[240:243], v[34:49]
	ds_read_b128 v[168:171], v179 offset:34144
	v_pk_fma_f16 v55, v55, s55, v233 op_sel_hi:[1,0,0]
	v_pk_fma_f16 v54, v54, s55, v233 op_sel_hi:[1,0,0]
	v_pk_max_f16 v53, v53, v55
	v_pk_max_f16 v52, v52, v54
	s_waitcnt lgkmcnt(5)
	v_mfma_f32_32x32x16_f16 v[34:49], v[118:121], v[244:247], v[34:49]
	ds_read_b128 v[240:243], v179 offset:34176
	v_cvt_pk_f16_f32 v172, v26, v27
	v_cvt_pk_f16_f32 v173, v28, v29
	v_mfma_f32_16x16x32_f16 v[62:65], v[70:73], v[50:53], 0
	s_waitcnt lgkmcnt(5)
	v_mfma_f32_32x32x16_f16 v[34:49], v[78:81], v[18:21], v[34:49]
	ds_read_b128 v[26:29], v179 offset:34208
	v_exp_f16_e64 v244, v172 clamp
	v_exp_f16_e64 v245, v173 clamp
	v_exp_f16_sdwa v244, v172 clamp dst_sel:WORD_1 dst_unused:UNUSED_PRESERVE src0_sel:WORD_1
	v_exp_f16_sdwa v245, v173 clamp dst_sel:WORD_1 dst_unused:UNUSED_PRESERVE src0_sel:WORD_1
	s_nop 0
	s_waitcnt lgkmcnt(5)
	v_mfma_f32_32x32x16_f16 v[34:49], v[102:105], v[248:251], v[34:49]
	ds_read_b128 v[18:21], v179 offset:34240
	v_pk_fma_f16 v245, v245, s55, v233 op_sel_hi:[1,0,0]
	s_nop 0
	v_pk_max_f16 v245, v173, v245
	v_pk_fma_f16 v173, v244, s55, v233 op_sel_hi:[1,0,0]
	s_nop 0
	v_pk_max_f16 v244, v172, v173
	s_waitcnt lgkmcnt(5)
	v_mfma_f32_32x32x16_f16 v[34:49], v[74:77], v[252:255], v[34:49]
	ds_read_b128 v[248:251], v179 offset:34272
	v_cvt_pk_f16_f32 v30, v30, v31
	v_cvt_pk_f16_f32 v31, v32, v33
	s_waitcnt lgkmcnt(5)
	v_mfma_f32_32x32x16_f16 v[34:49], v[106:109], v[22:25], v[34:49]
	v_exp_f16_e64 v32, v30 clamp
	v_exp_f16_e64 v33, v31 clamp
	v_exp_f16_sdwa v32, v30 clamp dst_sel:WORD_1 dst_unused:UNUSED_PRESERVE src0_sel:WORD_1
	v_exp_f16_sdwa v33, v31 clamp dst_sel:WORD_1 dst_unused:UNUSED_PRESERVE src0_sel:WORD_1
	s_nop 0
	s_waitcnt lgkmcnt(4)
	v_mfma_f32_32x32x16_f16 v[34:49], v[82:85], v[168:171], v[34:49]
	v_pk_fma_f16 v22, v33, s55, v233 op_sel_hi:[1,0,0]
	s_nop 0
	v_pk_max_f16 v247, v31, v22
	v_pk_fma_f16 v22, v32, s55, v233 op_sel_hi:[1,0,0]
	s_nop 0
	v_pk_max_f16 v246, v30, v22
	s_waitcnt lgkmcnt(3)
	v_mfma_f32_32x32x16_f16 v[34:49], v[110:113], v[240:243], v[34:49]
	s_waitcnt vmcnt(2)
	v_pk_add_f16 v24, v146, v158
	v_pk_add_f16 v25, v147, v159
	s_nop 0
	v_pk_mul_f16 v22, v160, v148 clamp
	v_pk_mul_f16 v23, v161, v149 clamp
	v_pk_max_f16 v22, v24, v22
	v_pk_max_f16 v23, v25, v23
	ds_write_b64 v189, v[22:23]
	v_mfma_f32_16x16x32_f16 v[62:65], v[66:69], v[244:247], v[62:65]
	s_waitcnt lgkmcnt(3)
	v_mfma_f32_32x32x16_f16 v[34:49], v[94:97], v[26:29], v[34:49]
	v_pk_add_f16 v24, v138, v158
	v_pk_add_f16 v25, v139, v159
	s_nop 0
	v_pk_mul_f16 v22, v160, v140 clamp
	v_pk_mul_f16 v23, v161, v141 clamp
	v_pk_max_f16 v22, v24, v22
	v_pk_max_f16 v23, v25, v23
	ds_write_b64 v189, v[22:23] offset:528
	s_waitcnt lgkmcnt(3)
	v_mfma_f32_32x32x16_f16 v[34:49], v[134:137], v[18:21], v[34:49]
	v_pk_add_f16 v24, v150, v158
	v_pk_add_f16 v25, v151, v159
	s_nop 0
	v_pk_mul_f16 v22, v160, v152 clamp
	v_pk_mul_f16 v23, v161, v153 clamp
	v_pk_max_f16 v22, v24, v22
	v_pk_max_f16 v23, v25, v23
	ds_write_b64 v189, v[22:23] offset:1056
	s_waitcnt lgkmcnt(3)
	v_mfma_f32_32x32x16_f16 v[34:49], v[130:133], v[248:251], v[34:49]
	v_pk_add_f16 v20, v142, v158
	v_pk_add_f16 v21, v143, v159
	s_nop 0
	v_pk_mul_f16 v18, v160, v144 clamp
	v_pk_mul_f16 v19, v161, v145 clamp
	v_pk_max_f16 v18, v20, v18
	v_pk_max_f16 v19, v21, v19
	ds_write_b64 v189, v[18:19] offset:1584
	ds_write2_b32 v201, v62, v63 offset1:1
	s_and_saveexec_b64 s[30:31], s[0:1]
	ds_write2_b32 v201, v64, v65 offset0:2 offset1:3
	s_or_b64 exec, exec, s[30:31]
	v_lshl_add_u64 v[166:167], s[20:21], 4, v[166:167]
	global_load_dwordx4 v[158:161], v[166:167], off
	ds_read_b128 v[50:53], v179 offset:50688
	ds_read_b128 v[54:57], v179 offset:50720
	ds_read_b128 v[58:61], v179 offset:50752
	ds_read_b128 v[62:65], v179 offset:50784
	ds_read_b128 v[168:171], v179 offset:50816
	ds_read_b128 v[240:243], v179 offset:50848
	s_waitcnt lgkmcnt(5)
	v_mfma_f32_32x32x16_f16 v[18:33], v[122:125], v[50:53], v[2:17]
	ds_read_b128 v[244:247], v179 offset:50880
	v_cvt_pk_f16_f32 v172, v34, v35
	v_cvt_pk_f16_f32 v173, v36, v37
	s_waitcnt lgkmcnt(5)
	v_mfma_f32_32x32x16_f16 v[18:33], v[98:101], v[54:57], v[18:33]
	ds_read_b128 v[34:37], v179 offset:50912
	v_exp_f16_e64 v50, v172 clamp
	v_exp_f16_e64 v51, v173 clamp
	v_exp_f16_sdwa v50, v172 clamp dst_sel:WORD_1 dst_unused:UNUSED_PRESERVE src0_sel:WORD_1
	v_exp_f16_sdwa v51, v173 clamp dst_sel:WORD_1 dst_unused:UNUSED_PRESERVE src0_sel:WORD_1
	s_nop 0
	s_waitcnt lgkmcnt(5)
	v_mfma_f32_32x32x16_f16 v[18:33], v[114:117], v[58:61], v[18:33]
	ds_read_b128 v[248:251], v179 offset:50944
	v_pk_fma_f16 v51, v51, s55, v233 op_sel_hi:[1,0,0]
	v_pk_fma_f16 v50, v50, s55, v233 op_sel_hi:[1,0,0]
	v_pk_max_f16 v51, v173, v51
	v_pk_max_f16 v50, v172, v50
	s_waitcnt lgkmcnt(5)
	v_mfma_f32_32x32x16_f16 v[18:33], v[86:89], v[62:65], v[18:33]
	ds_read_b128 v[252:255], v179 offset:50976
	v_cvt_pk_f16_f32 v52, v38, v39
	v_cvt_pk_f16_f32 v53, v40, v41
	s_waitcnt lgkmcnt(5)
	v_mfma_f32_32x32x16_f16 v[18:33], v[126:129], v[168:171], v[18:33]
	ds_read_b128 v[38:41], v179 offset:51008
	v_exp_f16_e64 v54, v52 clamp
	v_exp_f16_e64 v55, v53 clamp
	v_exp_f16_sdwa v54, v52 clamp dst_sel:WORD_1 dst_unused:UNUSED_PRESERVE src0_sel:WORD_1
	v_exp_f16_sdwa v55, v53 clamp dst_sel:WORD_1 dst_unused:UNUSED_PRESERVE src0_sel:WORD_1
	s_nop 0
	s_waitcnt lgkmcnt(5)
	v_mfma_f32_32x32x16_f16 v[18:33], v[90:93], v[240:243], v[18:33]
	ds_read_b128 v[168:171], v179 offset:51040
	v_pk_fma_f16 v55, v55, s55, v233 op_sel_hi:[1,0,0]
	v_pk_fma_f16 v54, v54, s55, v233 op_sel_hi:[1,0,0]
	v_pk_max_f16 v53, v53, v55
	v_pk_max_f16 v52, v52, v54
	s_waitcnt lgkmcnt(5)
	v_mfma_f32_32x32x16_f16 v[18:33], v[118:121], v[244:247], v[18:33]
	ds_read_b128 v[240:243], v179 offset:51072
	v_cvt_pk_f16_f32 v172, v42, v43
	v_cvt_pk_f16_f32 v173, v44, v45
	v_mfma_f32_16x16x32_f16 v[62:65], v[70:73], v[50:53], 0
	s_waitcnt lgkmcnt(5)
	v_mfma_f32_32x32x16_f16 v[18:33], v[78:81], v[34:37], v[18:33]
	ds_read_b128 v[42:45], v179 offset:51104
	v_exp_f16_e64 v244, v172 clamp
	v_exp_f16_e64 v245, v173 clamp
	v_exp_f16_sdwa v244, v172 clamp dst_sel:WORD_1 dst_unused:UNUSED_PRESERVE src0_sel:WORD_1
	v_exp_f16_sdwa v245, v173 clamp dst_sel:WORD_1 dst_unused:UNUSED_PRESERVE src0_sel:WORD_1
	s_nop 0
	s_waitcnt lgkmcnt(5)
	v_mfma_f32_32x32x16_f16 v[18:33], v[102:105], v[248:251], v[18:33]
	ds_read_b128 v[34:37], v179 offset:51136
	v_pk_fma_f16 v245, v245, s55, v233 op_sel_hi:[1,0,0]
	s_nop 0
	v_pk_max_f16 v245, v173, v245
	v_pk_fma_f16 v173, v244, s55, v233 op_sel_hi:[1,0,0]
	s_nop 0
	v_pk_max_f16 v244, v172, v173
	s_waitcnt lgkmcnt(5)
	v_mfma_f32_32x32x16_f16 v[18:33], v[74:77], v[252:255], v[18:33]
	ds_read_b128 v[248:251], v179 offset:51168
	v_cvt_pk_f16_f32 v46, v46, v47
	v_cvt_pk_f16_f32 v47, v48, v49
	s_waitcnt lgkmcnt(5)
	v_mfma_f32_32x32x16_f16 v[18:33], v[106:109], v[38:41], v[18:33]
	v_exp_f16_e64 v48, v46 clamp
	v_exp_f16_e64 v49, v47 clamp
	v_exp_f16_sdwa v48, v46 clamp dst_sel:WORD_1 dst_unused:UNUSED_PRESERVE src0_sel:WORD_1
	v_exp_f16_sdwa v49, v47 clamp dst_sel:WORD_1 dst_unused:UNUSED_PRESERVE src0_sel:WORD_1
	s_nop 0
	s_waitcnt lgkmcnt(4)
	v_mfma_f32_32x32x16_f16 v[18:33], v[82:85], v[168:171], v[18:33]
	v_pk_fma_f16 v38, v49, s55, v233 op_sel_hi:[1,0,0]
	s_nop 0
	v_pk_max_f16 v247, v47, v38
	v_pk_fma_f16 v38, v48, s55, v233 op_sel_hi:[1,0,0]
	s_nop 0
	v_pk_max_f16 v246, v46, v38
	s_waitcnt lgkmcnt(3)
	v_mfma_f32_32x32x16_f16 v[18:33], v[110:113], v[240:243], v[18:33]
	s_waitcnt vmcnt(2)
	v_pk_add_f16 v40, v146, v162
	v_pk_add_f16 v41, v147, v163
	s_nop 0
	v_pk_mul_f16 v38, v164, v148 clamp
	v_pk_mul_f16 v39, v165, v149 clamp
	v_pk_max_f16 v38, v40, v38
	v_pk_max_f16 v39, v41, v39
	ds_write_b64 v189, v[38:39] offset:16896
	v_mfma_f32_16x16x32_f16 v[62:65], v[66:69], v[244:247], v[62:65]
	s_waitcnt lgkmcnt(3)
	v_mfma_f32_32x32x16_f16 v[18:33], v[94:97], v[42:45], v[18:33]
	v_pk_add_f16 v40, v138, v162
	v_pk_add_f16 v41, v139, v163
	s_nop 0
	v_pk_mul_f16 v38, v164, v140 clamp
	v_pk_mul_f16 v39, v165, v141 clamp
	v_pk_max_f16 v38, v40, v38
	v_pk_max_f16 v39, v41, v39
	ds_write_b64 v189, v[38:39] offset:17424
	s_waitcnt lgkmcnt(3)
	v_mfma_f32_32x32x16_f16 v[18:33], v[134:137], v[34:37], v[18:33]
	v_pk_add_f16 v40, v150, v162
	v_pk_add_f16 v41, v151, v163
	s_nop 0
	v_pk_mul_f16 v38, v164, v152 clamp
	v_pk_mul_f16 v39, v165, v153 clamp
	v_pk_max_f16 v38, v40, v38
	v_pk_max_f16 v39, v41, v39
	ds_write_b64 v189, v[38:39] offset:17952
	v_pk_add_f16 v36, v142, v162
	v_pk_add_f16 v37, v143, v163
	s_nop 0
	v_pk_mul_f16 v34, v164, v144 clamp
	v_pk_mul_f16 v35, v165, v145 clamp
	v_pk_max_f16 v34, v36, v34
	v_pk_max_f16 v35, v37, v35
	ds_write_b64 v189, v[34:35] offset:18480
	ds_write2_b32 v211, v62, v63 offset1:1
	s_and_saveexec_b64 s[30:31], s[0:1]
	ds_write2_b32 v211, v64, v65 offset0:2 offset1:3
	s_or_b64 exec, exec, s[30:31]
	s_waitcnt lgkmcnt(6)
	v_mfma_f32_32x32x16_f16 v[18:33], v[130:133], v[248:251], v[18:33]
	s_add_i32 s35, s34, 1
	s_add_i32 s34, s56, 8
	s_cmp_eq_u32 s56, 8
	s_cselect_b64 vcc, -1, 0
	s_and_b64 s[30:31], vcc, exec
	v_lshl_add_u64 v[34:35], s[20:21], 4, v[166:167]
	s_cselect_b32 s20, s44, s20
	s_add_i32 s35, s35, 1
	s_and_b64 s[26:27], exec, s[26:27]
	s_cselect_b32 s30, s51, s35
	s_sub_i32 s26, 0x7e, s30
	s_mul_i32 s26, s26, 6
	s_ashr_i32 s27, s26, 31
	s_add_u32 s26, s28, s26
	s_addc_u32 s27, s29, s27
	s_add_i32 s31, s30, 1
	s_add_i32 s48, s48, 2
	s_add_i32 s54, s54, 16
	v_cndmask_b32_e32 v169, v35, v175, vcc
	v_cndmask_b32_e32 v168, v34, v174, vcc
	s_cmp_eq_u32 s34, 32
	s_waitcnt lgkmcnt(0)
	s_barrier
	s_cbranch_scc1 .LBB1_155
	ds_read_b128 v[50:53], v179
	ds_read_b128 v[54:57], v179 offset:32
	ds_read_b128 v[58:61], v179 offset:64
	ds_read_b128 v[62:65], v179 offset:96
	ds_read_b128 v[170:173], v179 offset:128
	ds_read_b128 v[240:243], v179 offset:160
	s_mov_b32 s56, s34
	s_and_b64 vcc, exec, s[8:9]
	s_cbranch_vccz .LBB1_42
	s_branch .LBB1_50

.LBB1_173:
	s_waitcnt lgkmcnt(5)
	v_mfma_f32_32x32x16_f16 v[34:49], v[122:125], v[50:53], v[2:17]
	ds_read_b128 v[170:173], v179 offset:192
	v_cvt_pk_f16_f32 v174, v18, v19
	v_cvt_pk_f16_f32 v175, v20, v21
	s_waitcnt lgkmcnt(5)
	v_mfma_f32_32x32x16_f16 v[34:49], v[98:101], v[54:57], v[34:49]
	ds_read_b128 v[18:21], v179 offset:224
	v_exp_f16_e64 v50, v174 clamp
	v_exp_f16_e64 v51, v175 clamp
	v_exp_f16_sdwa v50, v174 clamp dst_sel:WORD_1 dst_unused:UNUSED_PRESERVE src0_sel:WORD_1
	v_exp_f16_sdwa v51, v175 clamp dst_sel:WORD_1 dst_unused:UNUSED_PRESERVE src0_sel:WORD_1
	s_nop 0
	s_waitcnt lgkmcnt(5)
	v_mfma_f32_32x32x16_f16 v[34:49], v[114:117], v[58:61], v[34:49]
	ds_read_b128 v[230:233], v179 offset:256
	s_movk_i32 s20, 0x3dc5
	v_mov_b32_e32 v199, 0xbdc5
	v_pk_fma_f16 v51, v51, s20, v199 op_sel_hi:[1,0,0]
	v_pk_fma_f16 v50, v50, s20, v199 op_sel_hi:[1,0,0]
	v_pk_max_f16 v51, v175, v51
	v_pk_max_f16 v50, v174, v50
	s_waitcnt lgkmcnt(5)
	v_mfma_f32_32x32x16_f16 v[34:49], v[86:89], v[62:65], v[34:49]
	ds_read_b128 v[234:237], v179 offset:288
	v_cvt_pk_f16_f32 v52, v22, v23
	v_cvt_pk_f16_f32 v53, v24, v25
	s_waitcnt lgkmcnt(5)
	v_mfma_f32_32x32x16_f16 v[34:49], v[126:129], v[162:165], v[34:49]
	ds_read_b128 v[22:25], v179 offset:320
	v_exp_f16_e64 v54, v52 clamp
	v_exp_f16_e64 v55, v53 clamp
	v_exp_f16_sdwa v54, v52 clamp dst_sel:WORD_1 dst_unused:UNUSED_PRESERVE src0_sel:WORD_1
	v_exp_f16_sdwa v55, v53 clamp dst_sel:WORD_1 dst_unused:UNUSED_PRESERVE src0_sel:WORD_1
	s_nop 0
	s_waitcnt lgkmcnt(5)
	v_mfma_f32_32x32x16_f16 v[34:49], v[90:93], v[166:169], v[34:49]
	ds_read_b128 v[162:165], v179 offset:352
	v_pk_fma_f16 v55, v55, s20, v199 op_sel_hi:[1,0,0]
	v_pk_fma_f16 v54, v54, s20, v199 op_sel_hi:[1,0,0]
	v_pk_max_f16 v53, v53, v55
	v_pk_max_f16 v52, v52, v54
	s_waitcnt lgkmcnt(5)
	v_mfma_f32_32x32x16_f16 v[34:49], v[118:121], v[170:173], v[34:49]
	ds_read_b128 v[166:169], v179 offset:384
	v_cvt_pk_f16_f32 v170, v26, v27
	v_cvt_pk_f16_f32 v171, v28, v29
	v_mfma_f32_16x16x32_f16 v[62:65], v[70:73], v[50:53], 0
	s_waitcnt lgkmcnt(5)
	v_mfma_f32_32x32x16_f16 v[34:49], v[78:81], v[18:21], v[34:49]
	ds_read_b128 v[26:29], v179 offset:416
	v_exp_f16_e64 v172, v170 clamp
	v_exp_f16_e64 v173, v171 clamp
	v_exp_f16_sdwa v172, v170 clamp dst_sel:WORD_1 dst_unused:UNUSED_PRESERVE src0_sel:WORD_1
	v_exp_f16_sdwa v173, v171 clamp dst_sel:WORD_1 dst_unused:UNUSED_PRESERVE src0_sel:WORD_1
	s_nop 0
	s_waitcnt lgkmcnt(5)
	v_mfma_f32_32x32x16_f16 v[34:49], v[102:105], v[230:233], v[34:49]
	ds_read_b128 v[18:21], v179 offset:448
	v_pk_fma_f16 v173, v173, s20, v199 op_sel_hi:[1,0,0]
	v_pk_fma_f16 v172, v172, s20, v199 op_sel_hi:[1,0,0]
	v_pk_max_f16 v171, v171, v173
	v_pk_max_f16 v170, v170, v172
	s_waitcnt lgkmcnt(5)
	v_mfma_f32_32x32x16_f16 v[34:49], v[74:77], v[234:237], v[34:49]
	ds_read_b128 v[230:233], v179 offset:480
	v_cvt_pk_f16_f32 v30, v30, v31
	v_cvt_pk_f16_f32 v31, v32, v33
	s_waitcnt lgkmcnt(5)
	v_mfma_f32_32x32x16_f16 v[34:49], v[106:109], v[22:25], v[34:49]
	v_exp_f16_e64 v32, v30 clamp
	v_exp_f16_e64 v33, v31 clamp
	v_exp_f16_sdwa v32, v30 clamp dst_sel:WORD_1 dst_unused:UNUSED_PRESERVE src0_sel:WORD_1
	v_exp_f16_sdwa v33, v31 clamp dst_sel:WORD_1 dst_unused:UNUSED_PRESERVE src0_sel:WORD_1
	s_nop 0
	s_waitcnt lgkmcnt(4)
	v_mfma_f32_32x32x16_f16 v[34:49], v[82:85], v[162:165], v[34:49]
	v_pk_fma_f16 v22, v33, s20, v199 op_sel_hi:[1,0,0]
	s_nop 0
	v_pk_max_f16 v173, v31, v22
	v_pk_fma_f16 v22, v32, s20, v199 op_sel_hi:[1,0,0]
	s_nop 0
	v_pk_max_f16 v172, v30, v22
	s_waitcnt lgkmcnt(3)
	v_mfma_f32_32x32x16_f16 v[34:49], v[110:113], v[166:169], v[34:49]
	s_waitcnt vmcnt(1)
	v_pk_add_f16 v24, v146, v154
	v_pk_add_f16 v25, v147, v155
	s_nop 0
	v_pk_mul_f16 v22, v156, v148 clamp
	v_pk_mul_f16 v23, v157, v149 clamp
	v_pk_max_f16 v22, v24, v22
	v_pk_max_f16 v23, v25, v23
	ds_write_b64 v189, v[22:23] offset:33792
	v_mfma_f32_16x16x32_f16 v[62:65], v[66:69], v[170:173], v[62:65]
	s_waitcnt lgkmcnt(3)
	v_mfma_f32_32x32x16_f16 v[34:49], v[94:97], v[26:29], v[34:49]
	v_pk_add_f16 v24, v138, v154
	v_pk_add_f16 v25, v139, v155
	s_nop 0
	v_pk_mul_f16 v22, v156, v140 clamp
	v_pk_mul_f16 v23, v157, v141 clamp
	v_pk_max_f16 v22, v24, v22
	v_pk_max_f16 v23, v25, v23
	ds_write_b64 v189, v[22:23] offset:34320
	s_waitcnt lgkmcnt(3)
	v_mfma_f32_32x32x16_f16 v[34:49], v[134:137], v[18:21], v[34:49]
	v_pk_add_f16 v24, v150, v154
	v_pk_add_f16 v25, v151, v155
	s_nop 0
	v_pk_mul_f16 v22, v156, v152 clamp
	v_pk_mul_f16 v23, v157, v153 clamp
	v_pk_max_f16 v22, v24, v22
	v_pk_max_f16 v23, v25, v23
	ds_write_b64 v189, v[22:23] offset:34848
	s_waitcnt lgkmcnt(3)
	v_mfma_f32_32x32x16_f16 v[34:49], v[130:133], v[230:233], v[34:49]
	v_pk_add_f16 v20, v142, v154
	v_pk_add_f16 v21, v143, v155
	s_nop 0
	v_pk_mul_f16 v18, v156, v144 clamp
	v_pk_mul_f16 v19, v157, v145 clamp
	v_pk_max_f16 v18, v20, v18
	v_pk_max_f16 v19, v21, v19
	ds_write_b64 v189, v[18:19] offset:35376
	ds_write2_b32 v229, v62, v63 offset1:1
	s_and_saveexec_b64 s[20:21], s[0:1]
	ds_write2_b32 v229, v64, v65 offset0:2 offset1:3
	s_or_b64 exec, exec, s[20:21]
	ds_read_b128 v[50:53], v179 offset:16896
	ds_read_b128 v[54:57], v179 offset:16928
	ds_read_b128 v[58:61], v179 offset:16960
	ds_read_b128 v[62:65], v179 offset:16992
	ds_read_b128 v[154:157], v179 offset:17024
	ds_read_b128 v[162:165], v179 offset:17056
	s_waitcnt lgkmcnt(5)
	v_mfma_f32_32x32x16_f16 v[18:33], v[122:125], v[50:53], v[2:17]
	ds_read_b128 v[166:169], v179 offset:17088
	v_cvt_pk_f16_f32 v174, v34, v35
	v_cvt_pk_f16_f32 v175, v36, v37
	s_waitcnt lgkmcnt(5)
	v_mfma_f32_32x32x16_f16 v[18:33], v[98:101], v[54:57], v[18:33]
	ds_read_b128 v[34:37], v179 offset:17120
	v_exp_f16_e64 v50, v174 clamp
	v_exp_f16_e64 v51, v175 clamp
	v_exp_f16_sdwa v50, v174 clamp dst_sel:WORD_1 dst_unused:UNUSED_PRESERVE src0_sel:WORD_1
	v_exp_f16_sdwa v51, v175 clamp dst_sel:WORD_1 dst_unused:UNUSED_PRESERVE src0_sel:WORD_1
	s_nop 0
	s_waitcnt lgkmcnt(5)
	v_mfma_f32_32x32x16_f16 v[18:33], v[114:117], v[58:61], v[18:33]
	ds_read_b128 v[170:173], v179 offset:17152
	s_movk_i32 s20, 0x3dc5
	v_mov_b32_e32 v199, 0xbdc5
	v_pk_fma_f16 v51, v51, s20, v199 op_sel_hi:[1,0,0]
	v_pk_fma_f16 v50, v50, s20, v199 op_sel_hi:[1,0,0]
	v_pk_max_f16 v51, v175, v51
	v_pk_max_f16 v50, v174, v50
	s_waitcnt lgkmcnt(5)
	v_mfma_f32_32x32x16_f16 v[18:33], v[86:89], v[62:65], v[18:33]
	ds_read_b128 v[228:231], v179 offset:17184
	v_cvt_pk_f16_f32 v52, v38, v39
	v_cvt_pk_f16_f32 v53, v40, v41
	s_waitcnt lgkmcnt(5)
	v_mfma_f32_32x32x16_f16 v[18:33], v[126:129], v[154:157], v[18:33]
	ds_read_b128 v[38:41], v179 offset:17216
	v_exp_f16_e64 v54, v52 clamp
	v_exp_f16_e64 v55, v53 clamp
	v_exp_f16_sdwa v54, v52 clamp dst_sel:WORD_1 dst_unused:UNUSED_PRESERVE src0_sel:WORD_1
	v_exp_f16_sdwa v55, v53 clamp dst_sel:WORD_1 dst_unused:UNUSED_PRESERVE src0_sel:WORD_1
	s_nop 0
	s_waitcnt lgkmcnt(5)
	v_mfma_f32_32x32x16_f16 v[18:33], v[90:93], v[162:165], v[18:33]
	ds_read_b128 v[154:157], v179 offset:17248
	v_pk_fma_f16 v55, v55, s20, v199 op_sel_hi:[1,0,0]
	v_pk_fma_f16 v54, v54, s20, v199 op_sel_hi:[1,0,0]
	v_pk_max_f16 v53, v53, v55
	v_pk_max_f16 v52, v52, v54
	s_waitcnt lgkmcnt(5)
	v_mfma_f32_32x32x16_f16 v[18:33], v[118:121], v[166:169], v[18:33]
	ds_read_b128 v[162:165], v179 offset:17280
	v_cvt_pk_f16_f32 v166, v42, v43
	v_cvt_pk_f16_f32 v167, v44, v45
	v_mfma_f32_16x16x32_f16 v[62:65], v[70:73], v[50:53], 0
	s_waitcnt lgkmcnt(5)
	v_mfma_f32_32x32x16_f16 v[18:33], v[78:81], v[34:37], v[18:33]
	ds_read_b128 v[42:45], v179 offset:17312
	v_exp_f16_e64 v168, v166 clamp
	v_exp_f16_e64 v169, v167 clamp
	v_exp_f16_sdwa v168, v166 clamp dst_sel:WORD_1 dst_unused:UNUSED_PRESERVE src0_sel:WORD_1
	v_exp_f16_sdwa v169, v167 clamp dst_sel:WORD_1 dst_unused:UNUSED_PRESERVE src0_sel:WORD_1
	s_nop 0
	s_waitcnt lgkmcnt(5)
	v_mfma_f32_32x32x16_f16 v[18:33], v[102:105], v[170:173], v[18:33]
	ds_read_b128 v[34:37], v179 offset:17344
	v_pk_fma_f16 v169, v169, s20, v199 op_sel_hi:[1,0,0]
	v_pk_fma_f16 v168, v168, s20, v199 op_sel_hi:[1,0,0]
	v_pk_max_f16 v167, v167, v169
	v_pk_max_f16 v166, v166, v168
	s_waitcnt lgkmcnt(5)
	v_mfma_f32_32x32x16_f16 v[18:33], v[74:77], v[228:231], v[18:33]
	ds_read_b128 v[170:173], v179 offset:17376
	v_cvt_pk_f16_f32 v46, v46, v47
	v_cvt_pk_f16_f32 v47, v48, v49
	s_waitcnt lgkmcnt(5)
	v_mfma_f32_32x32x16_f16 v[18:33], v[106:109], v[38:41], v[18:33]
	v_exp_f16_e64 v48, v46 clamp
	v_exp_f16_e64 v49, v47 clamp
	v_exp_f16_sdwa v48, v46 clamp dst_sel:WORD_1 dst_unused:UNUSED_PRESERVE src0_sel:WORD_1
	v_exp_f16_sdwa v49, v47 clamp dst_sel:WORD_1 dst_unused:UNUSED_PRESERVE src0_sel:WORD_1
	s_nop 0
	s_waitcnt lgkmcnt(4)
	v_mfma_f32_32x32x16_f16 v[18:33], v[82:85], v[154:157], v[18:33]
	v_pk_fma_f16 v38, v49, s20, v199 op_sel_hi:[1,0,0]
	s_nop 0
	v_pk_max_f16 v169, v47, v38
	v_pk_fma_f16 v38, v48, s20, v199 op_sel_hi:[1,0,0]
	s_nop 0
	v_pk_max_f16 v168, v46, v38
	s_waitcnt lgkmcnt(3)
	v_mfma_f32_32x32x16_f16 v[18:33], v[110:113], v[162:165], v[18:33]
	s_waitcnt vmcnt(0)
	v_pk_add_f16 v40, v146, v158
	v_pk_add_f16 v41, v147, v159
	s_nop 0
	v_pk_mul_f16 v38, v160, v148 clamp
	v_pk_mul_f16 v39, v161, v149 clamp
	v_pk_max_f16 v38, v40, v38
	v_pk_max_f16 v39, v41, v39
	ds_write_b64 v189, v[38:39] offset:50688
	v_mfma_f32_16x16x32_f16 v[62:65], v[66:69], v[166:169], v[62:65]
	s_waitcnt lgkmcnt(3)
	v_mfma_f32_32x32x16_f16 v[18:33], v[94:97], v[42:45], v[18:33]
	v_pk_add_f16 v40, v138, v158
	v_pk_add_f16 v41, v139, v159
	s_nop 0
	v_pk_mul_f16 v38, v160, v140 clamp
	v_pk_mul_f16 v39, v161, v141 clamp
	v_pk_max_f16 v38, v40, v38
	v_pk_max_f16 v39, v41, v39
	ds_write_b64 v189, v[38:39] offset:51216
	s_waitcnt lgkmcnt(3)
	v_mfma_f32_32x32x16_f16 v[18:33], v[134:137], v[34:37], v[18:33]
	v_pk_add_f16 v40, v150, v158
	v_pk_add_f16 v41, v151, v159
	s_nop 0
	v_pk_mul_f16 v38, v160, v152 clamp
	v_pk_mul_f16 v39, v161, v153 clamp
	v_pk_max_f16 v38, v40, v38
	v_pk_max_f16 v39, v41, v39
	ds_write_b64 v189, v[38:39] offset:51744
	v_pk_add_f16 v36, v142, v158
	v_pk_add_f16 v37, v143, v159
	s_nop 0
	v_pk_mul_f16 v34, v160, v144 clamp
	v_pk_mul_f16 v35, v161, v145 clamp
	v_pk_max_f16 v34, v36, v34
	v_pk_max_f16 v35, v37, v35
	ds_write_b64 v189, v[34:35] offset:52272
	ds_write2_b32 v206, v62, v63 offset1:1
	s_and_saveexec_b64 s[20:21], s[0:1]
	ds_write2_b32 v206, v64, v65 offset0:2 offset1:3
	s_or_b64 exec, exec, s[20:21]
	s_waitcnt lgkmcnt(6)
	v_mfma_f32_32x32x16_f16 v[18:33], v[130:133], v[170:173], v[18:33]
	s_sub_i32 s20, 0x7c, s30
	s_mul_i32 s20, s20, 6
	s_ashr_i32 s21, s20, 31
	s_add_u32 s12, s12, s20
	s_addc_u32 s13, s13, s21
	s_and_b64 vcc, exec, s[8:9]
	s_waitcnt lgkmcnt(0)
	s_barrier
	s_cbranch_vccnz .LBB1_190
	s_cmp_lg_u32 s41, 0
	s_cbranch_scc0 .LBB1_186
	s_and_saveexec_b64 s[20:21], s[6:7]
	s_cbranch_execz .LBB1_185
	ds_read2_b32 v[34:35], v180 offset1:224
	v_add_u32_e32 v36, 0x700, v180
	v_add_u32_e32 v38, 0xe00, v180
	ds_read2_b32 v[36:37], v36 offset1:224
	ds_read2_b32 v[38:39], v38 offset1:224
	s_waitcnt lgkmcnt(2)
	v_add_f32_e32 v34, 0, v34
	v_add_f32_e32 v40, v34, v35
	v_add_u32_e32 v34, 0x1500, v180
	ds_read2_b32 v[34:35], v34 offset1:224
	s_waitcnt lgkmcnt(2)
	v_add_f32_e32 v36, v40, v36
	v_add_f32_e32 v36, v36, v37
	s_waitcnt lgkmcnt(1)
	v_add_f32_e32 v36, v36, v38
	v_add_f32_e32 v36, v36, v39
	s_waitcnt lgkmcnt(0)
	v_add_f32_e32 v34, v36, v34
	v_add_f32_e32 v34, v34, v35
	v_mov_b32_e32 v35, 0x19180
	v_lshl_add_u32 v35, v177, 2, v35
	ds_write_b32 v35, v34

.LBB1_199:
	ds_read_b128 v[50:53], v179 offset:33792
	ds_read_b128 v[54:57], v179 offset:33824
	ds_read_b128 v[58:61], v179 offset:33856
	ds_read_b128 v[62:65], v179 offset:33888
	ds_read_b128 v[138:141], v179 offset:33920
	ds_read_b128 v[142:145], v179 offset:33952
	s_waitcnt lgkmcnt(5)
	v_mfma_f32_32x32x16_f16 v[34:49], v[122:125], v[50:53], v[2:17]
	ds_read_b128 v[146:149], v179 offset:33984
	v_cvt_pk_f16_f32 v154, v18, v19
	v_cvt_pk_f16_f32 v155, v20, v21
	s_waitcnt lgkmcnt(5)
	v_mfma_f32_32x32x16_f16 v[34:49], v[98:101], v[54:57], v[34:49]
	ds_read_b128 v[18:21], v179 offset:34016
	v_exp_f16_e64 v50, v154 clamp
	v_exp_f16_e64 v51, v155 clamp
	v_exp_f16_sdwa v50, v154 clamp dst_sel:WORD_1 dst_unused:UNUSED_PRESERVE src0_sel:WORD_1
	v_exp_f16_sdwa v51, v155 clamp dst_sel:WORD_1 dst_unused:UNUSED_PRESERVE src0_sel:WORD_1
	s_nop 0
	s_waitcnt lgkmcnt(5)
	v_mfma_f32_32x32x16_f16 v[34:49], v[114:117], v[58:61], v[34:49]
	ds_read_b128 v[150:153], v179 offset:34048
	s_movk_i32 s20, 0x3dc5
	v_mov_b32_e32 v158, 0xbdc5
	v_pk_fma_f16 v51, v51, s20, v158 op_sel_hi:[1,0,0]
	v_pk_fma_f16 v50, v50, s20, v158 op_sel_hi:[1,0,0]
	v_pk_max_f16 v51, v155, v51
	v_pk_max_f16 v50, v154, v50
	s_waitcnt lgkmcnt(5)
	v_mfma_f32_32x32x16_f16 v[34:49], v[86:89], v[62:65], v[34:49]
	ds_read_b128 v[154:157], v179 offset:34080
	v_cvt_pk_f16_f32 v52, v22, v23
	v_cvt_pk_f16_f32 v53, v24, v25
	s_waitcnt lgkmcnt(5)
	v_mfma_f32_32x32x16_f16 v[34:49], v[126:129], v[138:141], v[34:49]
	ds_read_b128 v[22:25], v179 offset:34112
	v_exp_f16_e64 v54, v52 clamp
	v_exp_f16_e64 v55, v53 clamp
	v_exp_f16_sdwa v54, v52 clamp dst_sel:WORD_1 dst_unused:UNUSED_PRESERVE src0_sel:WORD_1
	v_exp_f16_sdwa v55, v53 clamp dst_sel:WORD_1 dst_unused:UNUSED_PRESERVE src0_sel:WORD_1
	s_nop 0
	s_waitcnt lgkmcnt(5)
	v_mfma_f32_32x32x16_f16 v[34:49], v[90:93], v[142:145], v[34:49]
	ds_read_b128 v[138:141], v179 offset:34144
	v_pk_fma_f16 v55, v55, s20, v158 op_sel_hi:[1,0,0]
	v_pk_fma_f16 v54, v54, s20, v158 op_sel_hi:[1,0,0]
	v_pk_max_f16 v53, v53, v55
	v_pk_max_f16 v52, v52, v54
	s_waitcnt lgkmcnt(5)
	v_mfma_f32_32x32x16_f16 v[34:49], v[118:121], v[146:149], v[34:49]
	ds_read_b128 v[142:145], v179 offset:34176
	v_cvt_pk_f16_f32 v146, v26, v27
	v_cvt_pk_f16_f32 v147, v28, v29
	v_mfma_f32_16x16x32_f16 v[62:65], v[70:73], v[50:53], 0
	s_waitcnt lgkmcnt(5)
	v_mfma_f32_32x32x16_f16 v[34:49], v[78:81], v[18:21], v[34:49]
	ds_read_b128 v[26:29], v179 offset:34208
	v_exp_f16_e64 v148, v146 clamp
	v_exp_f16_e64 v149, v147 clamp
	v_exp_f16_sdwa v148, v146 clamp dst_sel:WORD_1 dst_unused:UNUSED_PRESERVE src0_sel:WORD_1
	v_exp_f16_sdwa v149, v147 clamp dst_sel:WORD_1 dst_unused:UNUSED_PRESERVE src0_sel:WORD_1
	s_nop 0
	s_waitcnt lgkmcnt(5)
	v_mfma_f32_32x32x16_f16 v[34:49], v[102:105], v[150:153], v[34:49]
	ds_read_b128 v[18:21], v179 offset:34240
	v_pk_fma_f16 v149, v149, s20, v158 op_sel_hi:[1,0,0]
	v_pk_fma_f16 v148, v148, s20, v158 op_sel_hi:[1,0,0]
	v_pk_max_f16 v147, v147, v149
	v_pk_max_f16 v146, v146, v148
	s_waitcnt lgkmcnt(5)
	v_mfma_f32_32x32x16_f16 v[34:49], v[74:77], v[154:157], v[34:49]
	ds_read_b128 v[150:153], v179 offset:34272
	v_cvt_pk_f16_f32 v30, v30, v31
	v_cvt_pk_f16_f32 v31, v32, v33
	s_waitcnt lgkmcnt(5)
	v_mfma_f32_32x32x16_f16 v[34:49], v[106:109], v[22:25], v[34:49]
	v_exp_f16_e64 v32, v30 clamp
	v_exp_f16_e64 v33, v31 clamp
	v_exp_f16_sdwa v32, v30 clamp dst_sel:WORD_1 dst_unused:UNUSED_PRESERVE src0_sel:WORD_1
	v_exp_f16_sdwa v33, v31 clamp dst_sel:WORD_1 dst_unused:UNUSED_PRESERVE src0_sel:WORD_1
	s_nop 0
	s_waitcnt lgkmcnt(4)
	v_mfma_f32_32x32x16_f16 v[34:49], v[82:85], v[138:141], v[34:49]
	v_pk_fma_f16 v22, v33, s20, v158 op_sel_hi:[1,0,0]
	s_nop 0
	v_pk_max_f16 v149, v31, v22
	v_pk_fma_f16 v22, v32, s20, v158 op_sel_hi:[1,0,0]
	s_nop 0
	v_pk_max_f16 v148, v30, v22
	s_waitcnt lgkmcnt(3)
	v_mfma_f32_32x32x16_f16 v[34:49], v[110:113], v[142:145], v[34:49]
	v_mfma_f32_16x16x32_f16 v[62:65], v[66:69], v[146:149], v[62:65]
	s_waitcnt lgkmcnt(2)
	v_mfma_f32_32x32x16_f16 v[34:49], v[94:97], v[26:29], v[34:49]
	s_waitcnt lgkmcnt(1)
	v_mfma_f32_32x32x16_f16 v[34:49], v[134:137], v[18:21], v[34:49]
	s_waitcnt lgkmcnt(0)
	v_mfma_f32_32x32x16_f16 v[34:49], v[130:133], v[150:153], v[34:49]
	s_nop 5
	ds_write2_b32 v201, v62, v63 offset1:1
	s_and_saveexec_b64 s[20:21], s[0:1]
	ds_write2_b32 v201, v64, v65 offset0:2 offset1:3
	s_or_b64 exec, exec, s[20:21]
	ds_read_b128 v[18:21], v179 offset:50688
	ds_read_b128 v[22:25], v179 offset:50720
	ds_read_b128 v[26:29], v179 offset:50752
	ds_read_b128 v[30:33], v179 offset:50784
	ds_read_b128 v[50:53], v179 offset:50816
	ds_read_b128 v[54:57], v179 offset:50848
	s_waitcnt lgkmcnt(5)
	v_mfma_f32_32x32x16_f16 v[2:17], v[122:125], v[18:21], v[2:17]
	ds_read_b128 v[58:61], v179 offset:50880
	v_cvt_pk_f16_f32 v138, v34, v35
	v_cvt_pk_f16_f32 v139, v36, v37
	s_waitcnt lgkmcnt(5)
	v_mfma_f32_32x32x16_f16 v[2:17], v[98:101], v[22:25], v[2:17]
	ds_read_b128 v[34:37], v179 offset:50912
	v_exp_f16_e64 v18, v138 clamp
	v_exp_f16_e64 v19, v139 clamp
	v_exp_f16_sdwa v18, v138 clamp dst_sel:WORD_1 dst_unused:UNUSED_PRESERVE src0_sel:WORD_1
	v_exp_f16_sdwa v19, v139 clamp dst_sel:WORD_1 dst_unused:UNUSED_PRESERVE src0_sel:WORD_1
	s_nop 0
	s_waitcnt lgkmcnt(5)
	v_mfma_f32_32x32x16_f16 v[2:17], v[114:117], v[26:29], v[2:17]
	ds_read_b128 v[62:65], v179 offset:50944
	s_movk_i32 s20, 0x3dc5
	v_mov_b32_e32 v122, 0xbdc5
	v_pk_fma_f16 v19, v19, s20, v122 op_sel_hi:[1,0,0]
	v_pk_fma_f16 v18, v18, s20, v122 op_sel_hi:[1,0,0]
	v_pk_max_f16 v19, v139, v19
	v_pk_max_f16 v18, v138, v18
	s_waitcnt lgkmcnt(5)
	v_mfma_f32_32x32x16_f16 v[2:17], v[86:89], v[30:33], v[2:17]
	ds_read_b128 v[98:101], v179 offset:50976
	v_cvt_pk_f16_f32 v20, v38, v39
	v_cvt_pk_f16_f32 v21, v40, v41
	s_waitcnt lgkmcnt(5)
	v_mfma_f32_32x32x16_f16 v[2:17], v[126:129], v[50:53], v[2:17]
	ds_read_b128 v[38:41], v179 offset:51008
	v_exp_f16_e64 v22, v20 clamp
	v_exp_f16_e64 v23, v21 clamp
	v_exp_f16_sdwa v22, v20 clamp dst_sel:WORD_1 dst_unused:UNUSED_PRESERVE src0_sel:WORD_1
	v_exp_f16_sdwa v23, v21 clamp dst_sel:WORD_1 dst_unused:UNUSED_PRESERVE src0_sel:WORD_1
	s_nop 0
	s_waitcnt lgkmcnt(5)
	v_mfma_f32_32x32x16_f16 v[2:17], v[90:93], v[54:57], v[2:17]
	ds_read_b128 v[50:53], v179 offset:51040
	v_pk_fma_f16 v23, v23, s20, v122 op_sel_hi:[1,0,0]
	v_pk_fma_f16 v22, v22, s20, v122 op_sel_hi:[1,0,0]
	v_pk_max_f16 v21, v21, v23
	v_pk_max_f16 v20, v20, v22
	s_waitcnt lgkmcnt(5)
	v_mfma_f32_32x32x16_f16 v[2:17], v[118:121], v[58:61], v[2:17]
	ds_read_b128 v[54:57], v179 offset:51072
	v_cvt_pk_f16_f32 v58, v42, v43
	v_cvt_pk_f16_f32 v59, v44, v45
	v_mfma_f32_16x16x32_f16 v[30:33], v[70:73], v[18:21], 0
	s_waitcnt lgkmcnt(5)
	v_mfma_f32_32x32x16_f16 v[2:17], v[78:81], v[34:37], v[2:17]
	ds_read_b128 v[42:45], v179 offset:51104
	v_exp_f16_e64 v60, v58 clamp
	v_exp_f16_e64 v61, v59 clamp
	v_exp_f16_sdwa v60, v58 clamp dst_sel:WORD_1 dst_unused:UNUSED_PRESERVE src0_sel:WORD_1
	v_exp_f16_sdwa v61, v59 clamp dst_sel:WORD_1 dst_unused:UNUSED_PRESERVE src0_sel:WORD_1
	s_nop 0
	s_waitcnt lgkmcnt(5)
	v_mfma_f32_32x32x16_f16 v[2:17], v[102:105], v[62:65], v[2:17]
	ds_read_b128 v[34:37], v179 offset:51136
	v_pk_fma_f16 v61, v61, s20, v122 op_sel_hi:[1,0,0]
	v_pk_fma_f16 v60, v60, s20, v122 op_sel_hi:[1,0,0]
	v_pk_max_f16 v59, v59, v61
	v_pk_max_f16 v58, v58, v60
	s_waitcnt lgkmcnt(5)
	v_mfma_f32_32x32x16_f16 v[2:17], v[74:77], v[98:101], v[2:17]
	ds_read_b128 v[62:65], v179 offset:51168
	v_cvt_pk_f16_f32 v46, v46, v47
	v_cvt_pk_f16_f32 v47, v48, v49
	s_waitcnt lgkmcnt(5)
	v_mfma_f32_32x32x16_f16 v[2:17], v[106:109], v[38:41], v[2:17]
	v_exp_f16_e64 v48, v46 clamp
	v_exp_f16_e64 v49, v47 clamp
	v_exp_f16_sdwa v48, v46 clamp dst_sel:WORD_1 dst_unused:UNUSED_PRESERVE src0_sel:WORD_1
	v_exp_f16_sdwa v49, v47 clamp dst_sel:WORD_1 dst_unused:UNUSED_PRESERVE src0_sel:WORD_1
	s_nop 0
	s_waitcnt lgkmcnt(4)
	v_mfma_f32_32x32x16_f16 v[2:17], v[82:85], v[50:53], v[2:17]
	v_pk_fma_f16 v38, v49, s20, v122 op_sel_hi:[1,0,0]
	s_nop 0
	v_pk_max_f16 v61, v47, v38
	v_pk_fma_f16 v38, v48, s20, v122 op_sel_hi:[1,0,0]
	s_nop 0
	v_pk_max_f16 v60, v46, v38
	s_waitcnt lgkmcnt(3)
	v_mfma_f32_32x32x16_f16 v[2:17], v[110:113], v[54:57], v[2:17]
	v_mfma_f32_16x16x32_f16 v[30:33], v[66:69], v[58:61], v[30:33]
	s_waitcnt lgkmcnt(2)
	v_mfma_f32_32x32x16_f16 v[2:17], v[94:97], v[42:45], v[2:17]
	s_waitcnt lgkmcnt(1)
	v_mfma_f32_32x32x16_f16 v[2:17], v[134:137], v[34:37], v[2:17]
	s_nop 5
	ds_write2_b32 v211, v30, v31 offset1:1
	s_and_saveexec_b64 s[20:21], s[0:1]
	ds_write2_b32 v211, v32, v33 offset0:2 offset1:3
	s_or_b64 exec, exec, s[20:21]
	s_waitcnt lgkmcnt(2)
	v_mfma_f32_32x32x16_f16 v[2:17], v[130:133], v[62:65], v[2:17]
	s_sub_i32 s20, 0x7a, s30
	s_mul_i32 s20, s20, 6
	s_ashr_i32 s21, s20, 31
	s_add_u32 s12, s12, s20
	s_addc_u32 s13, s13, s21
	s_and_b64 vcc, exec, s[8:9]
	s_waitcnt lgkmcnt(0)
	s_barrier
	s_cbranch_vccnz .LBB1_216
	s_cmp_lg_u32 s41, 0
	s_cbranch_scc0 .LBB1_212
	s_and_saveexec_b64 s[20:21], s[6:7]
	s_cbranch_execz .LBB1_211
	ds_read2_b32 v[18:19], v200 offset1:224
	v_add_u32_e32 v20, 0x700, v200
	v_add_u32_e32 v22, 0xe00, v200
	ds_read2_b32 v[20:21], v20 offset1:224
	ds_read2_b32 v[22:23], v22 offset1:224
	s_waitcnt lgkmcnt(2)
	v_add_f32_e32 v18, 0, v18
	v_add_f32_e32 v24, v18, v19
	v_add_u32_e32 v18, 0x1500, v200
	ds_read2_b32 v[18:19], v18 offset1:224
	s_waitcnt lgkmcnt(2)
	v_add_f32_e32 v20, v24, v20
	v_add_f32_e32 v20, v20, v21
	s_waitcnt lgkmcnt(1)
	v_add_f32_e32 v20, v20, v22
	v_add_f32_e32 v20, v20, v23
	s_waitcnt lgkmcnt(0)
	v_add_f32_e32 v18, v20, v18
	v_add_f32_e32 v18, v18, v19
	v_mov_b32_e32 v19, 0x19280
	v_lshl_add_u32 v19, v177, 2, v19
	ds_write_b32 v19, v18
